# v81 + nt on the 64 output stores of the final RMSNorm pass of P12 (last writes of the kernel)
# speedup vs baseline: 1.0382x; 1.0042x over previous
; #define P12_VISSUE(c_, i_, q_, D_X) do { _Pragma("unroll") for (int b = 0; b < 8; ++b) { const int idx = ((q_) * 8 + b) * 4 + eg; const unsigned ro = (unsigned)(c_) * 16384u + (unsigned)EL[(i_) * 128 + idx]; \
;           const v3u_ ld_ = *(const v3u_*)(V8 + (size_t)(ro * 192u + 12u * (unsigned)cl)); if (b & 1) D_X[b >> 1].hi = ld_; else D_X[b >> 1].lo = ld_; } } while (0)
; __device__ __forceinline__ void p12_peer(Frame& F) {
;     ...
;       v6u_ dA[4], dB[4];
;       P12_VISSUE(0, 0, 0, dA);
; _Pragma("nounroll")
;       for (int c = 0; c < 16; ++c) {
;           int lo_ = 16 * cl + 4 * eg; asm volatile("" : "+v"(lo_));
; _Pragma("nounroll")
;           for (int i = 0; i < 4; ++i) { const int t = F.gw + i * F.NGW;
;               f32x2 acc2[8];
; #pragma unroll
;               for (int m = 0; m < 8; ++m) acc2[m] = (f32x2){0.f, 0.f};
;               const v2u hb = *(const v2u*)(HN + ((size_t)t * D_ + (size_t)(unsigned)(256 * c + lo_)));
;               P12_VISSUE(c, i, 1, dB); asm volatile("" ::: "memory"); P12_VCOMP(i, 0, dA);
;               P12_VISSUE(c, i, 2, dA); asm volatile("" ::: "memory"); P12_VCOMP(i, 1, dB);
;               P12_VISSUE(c, i, 3, dB); asm volatile("" ::: "memory"); P12_VCOMP(i, 2, dA);
;               { const int in_ = i + 1 < 4 ? i + 1 : 0, cn_ = i + 1 < 4 ? c : (c + 1 < 16 ? c + 1 : 15); P12_VISSUE(cn_, in_, 0, dA); } asm volatile("" ::: "memory"); P12_VCOMP(i, 3, dB);
.LBB0_3403:
	v_add_u32_e32 v152, s28, v175
	ds_read_u16 v2, v152
	ds_read_u16 v3, v152 offset:8
	ds_read_u16 v4, v152 offset:16
	ds_read_u16 v5, v152 offset:24
	ds_read_u16 v6, v152 offset:32
	ds_read_u16 v7, v152 offset:40
	ds_read_u16 v8, v152 offset:48
	ds_read_u16 v9, v152 offset:56
	s_ashr_i32 s13, s12, 31
	s_lshl_b64 s[14:15], s[12:13], 13
	v_lshl_add_u64 v[0:1], v[164:165], 0, s[14:15]
	s_cmpk_eq_i32 s28, 0x300
	global_load_dwordx2 v[158:159], v[0:1], off
	s_cselect_b32 s30, 0, s23
	s_waitcnt lgkmcnt(7)
	v_add_u32_e32 v0, s21, v2
	v_lshl_add_u32 v179, s30, 1, v161
	s_waitcnt lgkmcnt(6)
	v_add_u32_e32 v2, s21, v3
	s_waitcnt lgkmcnt(5)
	v_add_u32_e32 v4, s21, v4
	s_waitcnt lgkmcnt(4)
	v_add_u32_e32 v10, s21, v5
	s_waitcnt lgkmcnt(3)
	v_add_u32_e32 v11, s21, v6
	s_waitcnt lgkmcnt(2)
	v_add_u32_e32 v12, s21, v7
	s_waitcnt lgkmcnt(1)
	v_add_u32_e32 v13, s21, v8
	s_waitcnt lgkmcnt(0)
	v_add_u32_e32 v14, s21, v9
	v_mad_u64_u32 v[0:1], s[30:31], v0, s16, v[160:161]
	v_mad_u64_u32 v[2:3], s[30:31], v2, s16, v[160:161]
	v_mad_u64_u32 v[4:5], s[30:31], v4, s16, v[160:161]
	v_mad_u64_u32 v[6:7], s[30:31], v10, s16, v[160:161]
	v_mad_u64_u32 v[8:9], s[30:31], v11, s16, v[160:161]
	v_mad_u64_u32 v[10:11], s[30:31], v12, s16, v[160:161]
	v_mad_u64_u32 v[12:13], s[30:31], v13, s16, v[160:161]
	v_mad_u64_u32 v[14:15], s[30:31], v14, s16, v[160:161]
	global_load_dwordx3 v[154:156], v0, s[2:3]
	global_load_dwordx3 v[220:222], v2, s[2:3]
	global_load_dwordx3 v[180:182], v4, s[2:3]
	global_load_dwordx3 v[224:226], v6, s[2:3]
	global_load_dwordx3 v[186:188], v8, s[2:3]
	global_load_dwordx3 v[228:230], v10, s[2:3]
	global_load_dwordx3 v[192:194], v12, s[2:3]
	global_load_dwordx3 v[232:234], v14, s[2:3]
	ds_read2_b32 v[166:167], v177 offset1:4
	ds_read2_b32 v[168:169], v177 offset0:8 offset1:12
	s_waitcnt vmcnt(10)
	ds_read2_b32 v[184:185], v177 offset0:16 offset1:20
	s_waitcnt vmcnt(9)
	ds_read2_b32 v[190:191], v177 offset0:24 offset1:28
	v_cvt_scalef32_pk32_f32_fp6 v[96:127], v[134:139], 1.0
	v_cvt_scalef32_pk32_f32_fp6 v[64:95], v[128:133], 1.0
	ds_read_u16 v129, v152 offset:64
	ds_read_u16 v131, v152 offset:72
	ds_read_u16 v132, v152 offset:80
	ds_read_u16 v133, v152 offset:88
	ds_read_u16 v134, v152 offset:96
	ds_read_u16 v135, v152 offset:104
	ds_read_u16 v136, v152 offset:112
	ds_read_u16 v137, v152 offset:120
	s_waitcnt lgkmcnt(11)
	v_pk_fma_f32 v[96:97], v[96:97], v[166:167], 0 op_sel_hi:[1,0,0]
	v_pk_fma_f32 v[98:99], v[98:99], v[166:167], 0 op_sel_hi:[1,0,0]
	v_pk_fma_f32 v[100:101], v[100:101], v[166:167], 0 op_sel_hi:[1,0,0]
	v_pk_fma_f32 v[102:103], v[102:103], v[166:167], 0 op_sel_hi:[1,0,0]
	v_pk_fma_f32 v[104:105], v[104:105], v[166:167], 0 op_sel_hi:[1,0,0]
	v_pk_fma_f32 v[106:107], v[106:107], v[166:167], 0 op_sel_hi:[1,0,0]
	v_pk_fma_f32 v[108:109], v[108:109], v[166:167], 0 op_sel_hi:[1,0,0]
	v_pk_fma_f32 v[110:111], v[110:111], v[166:167], 0 op_sel_hi:[1,0,0]
	v_mov_b32_e32 v128, v167
	s_waitcnt lgkmcnt(7)
	v_pk_fma_f32 v[96:97], v[112:113], v[128:129], v[96:97] op_sel_hi:[1,0,1]
	v_pk_fma_f32 v[98:99], v[114:115], v[128:129], v[98:99] op_sel_hi:[1,0,1]
	v_pk_fma_f32 v[100:101], v[116:117], v[128:129], v[100:101] op_sel_hi:[1,0,1]
	v_pk_fma_f32 v[102:103], v[118:119], v[128:129], v[102:103] op_sel_hi:[1,0,1]
	v_pk_fma_f32 v[104:105], v[120:121], v[128:129], v[104:105] op_sel_hi:[1,0,1]
	v_pk_fma_f32 v[106:107], v[122:123], v[128:129], v[106:107] op_sel_hi:[1,0,1]
	v_pk_fma_f32 v[108:109], v[124:125], v[128:129], v[108:109] op_sel_hi:[1,0,1]
	v_pk_fma_f32 v[110:111], v[126:127], v[128:129], v[110:111] op_sel_hi:[1,0,1]
	v_add_u32_e32 v112, s21, v129
	v_mov_b32_e32 v130, v169
	s_waitcnt lgkmcnt(6)
	v_add_u32_e32 v113, s21, v131
	s_waitcnt lgkmcnt(5)
	v_add_u32_e32 v114, s21, v132
	s_waitcnt lgkmcnt(4)
	v_add_u32_e32 v115, s21, v133
	s_waitcnt lgkmcnt(3)
	v_add_u32_e32 v116, s21, v134
	s_waitcnt lgkmcnt(2)
	v_add_u32_e32 v117, s21, v135
	s_waitcnt lgkmcnt(1)
	v_add_u32_e32 v118, s21, v136
	s_waitcnt lgkmcnt(0)
	v_add_u32_e32 v119, s21, v137
	v_pk_fma_f32 v[64:65], v[64:65], v[168:169], v[96:97] op_sel_hi:[1,0,1]
	v_pk_fma_f32 v[66:67], v[66:67], v[168:169], v[98:99] op_sel_hi:[1,0,1]
	v_pk_fma_f32 v[68:69], v[68:69], v[168:169], v[100:101] op_sel_hi:[1,0,1]
	v_pk_fma_f32 v[70:71], v[70:71], v[168:169], v[102:103] op_sel_hi:[1,0,1]
	v_pk_fma_f32 v[72:73], v[72:73], v[168:169], v[104:105] op_sel_hi:[1,0,1]
	v_pk_fma_f32 v[74:75], v[74:75], v[168:169], v[106:107] op_sel_hi:[1,0,1]
	v_pk_fma_f32 v[76:77], v[76:77], v[168:169], v[108:109] op_sel_hi:[1,0,1]
	v_pk_fma_f32 v[78:79], v[78:79], v[168:169], v[110:111] op_sel_hi:[1,0,1]
	v_mad_u64_u32 v[96:97], s[30:31], v112, s16, v[160:161]
	v_cvt_scalef32_pk32_f32_fp6 v[32:63], v[140:145], 1.0
	v_mad_u64_u32 v[98:99], s[30:31], v113, s16, v[160:161]
	v_mad_u64_u32 v[100:101], s[30:31], v114, s16, v[160:161]
	v_mad_u64_u32 v[102:103], s[30:31], v115, s16, v[160:161]
	v_mad_u64_u32 v[104:105], s[30:31], v116, s16, v[160:161]
	v_mad_u64_u32 v[106:107], s[30:31], v117, s16, v[160:161]
	v_mad_u64_u32 v[108:109], s[30:31], v118, s16, v[160:161]
	v_mad_u64_u32 v[110:111], s[30:31], v119, s16, v[160:161]
	v_pk_fma_f32 v[64:65], v[80:81], v[130:131], v[64:65] op_sel_hi:[1,0,1]
	v_pk_fma_f32 v[66:67], v[82:83], v[130:131], v[66:67] op_sel_hi:[1,0,1]
	v_pk_fma_f32 v[68:69], v[84:85], v[130:131], v[68:69] op_sel_hi:[1,0,1]
	v_pk_fma_f32 v[70:71], v[86:87], v[130:131], v[70:71] op_sel_hi:[1,0,1]
	v_pk_fma_f32 v[72:73], v[88:89], v[130:131], v[72:73] op_sel_hi:[1,0,1]
	v_pk_fma_f32 v[74:75], v[90:91], v[130:131], v[74:75] op_sel_hi:[1,0,1]
	v_pk_fma_f32 v[76:77], v[92:93], v[130:131], v[76:77] op_sel_hi:[1,0,1]
; #define P12_VISSUE(c_, i_, q_, D_X) do { _Pragma("unroll") for (int b = 0; b < 8; ++b) { const int idx = ((q_) * 8 + b) * 4 + eg; const unsigned ro = (unsigned)(c_) * 16384u + (unsigned)EL[(i_) * 128 + idx]; \
;           const v3u_ ld_ = *(const v3u_*)(V8 + (size_t)(ro * 192u + 12u * (unsigned)cl)); if (b & 1) D_X[b >> 1].hi = ld_; else D_X[b >> 1].lo = ld_; } } while (0)
; __device__ __forceinline__ void p12_peer(Frame& F) {
;     ...
;       v6u_ dA[4], dB[4];
;       P12_VISSUE(0, 0, 0, dA);
; _Pragma("nounroll")
;       for (int c = 0; c < 16; ++c) {
;           int lo_ = 16 * cl + 4 * eg; asm volatile("" : "+v"(lo_));
; _Pragma("nounroll")
;           for (int i = 0; i < 4; ++i) { const int t = F.gw + i * F.NGW;
;               f32x2 acc2[8];
; #pragma unroll
;               for (int m = 0; m < 8; ++m) acc2[m] = (f32x2){0.f, 0.f};
;               const v2u hb = *(const v2u*)(HN + ((size_t)t * D_ + (size_t)(unsigned)(256 * c + lo_)));
;               P12_VISSUE(c, i, 1, dB); asm volatile("" ::: "memory"); P12_VCOMP(i, 0, dA);
;               P12_VISSUE(c, i, 2, dA); asm volatile("" ::: "memory"); P12_VCOMP(i, 1, dB);
;               P12_VISSUE(c, i, 3, dB); asm volatile("" ::: "memory"); P12_VCOMP(i, 2, dA);
;               { const int in_ = i + 1 < 4 ? i + 1 : 0, cn_ = i + 1 < 4 ? c : (c + 1 < 16 ? c + 1 : 15); P12_VISSUE(cn_, in_, 0, dA); } asm volatile("" ::: "memory"); P12_VCOMP(i, 3, dB);
	v_pk_fma_f32 v[78:79], v[94:95], v[130:131], v[78:79] op_sel_hi:[1,0,1]
	global_load_dwordx3 v[198:200], v96, s[2:3]
	global_load_dwordx3 v[128:130], v98, s[2:3]
	global_load_dwordx3 v[204:206], v100, s[2:3]
	global_load_dwordx3 v[132:134], v102, s[2:3]
	global_load_dwordx3 v[210:212], v104, s[2:3]
	global_load_dwordx3 v[136:138], v106, s[2:3]
	global_load_dwordx3 v[216:218], v108, s[2:3]
	global_load_dwordx3 v[140:142], v110, s[2:3]
	v_mov_b32_e32 v144, v185
	v_pk_fma_f32 v[32:33], v[32:33], v[184:185], v[64:65] op_sel_hi:[1,0,1]
	v_pk_fma_f32 v[34:35], v[34:35], v[184:185], v[66:67] op_sel_hi:[1,0,1]
	v_pk_fma_f32 v[36:37], v[36:37], v[184:185], v[68:69] op_sel_hi:[1,0,1]
	v_pk_fma_f32 v[38:39], v[38:39], v[184:185], v[70:71] op_sel_hi:[1,0,1]
	v_pk_fma_f32 v[40:41], v[40:41], v[184:185], v[72:73] op_sel_hi:[1,0,1]
	v_pk_fma_f32 v[42:43], v[42:43], v[184:185], v[74:75] op_sel_hi:[1,0,1]
	v_pk_fma_f32 v[44:45], v[44:45], v[184:185], v[76:77] op_sel_hi:[1,0,1]
	v_pk_fma_f32 v[46:47], v[46:47], v[184:185], v[78:79] op_sel_hi:[1,0,1]
	v_cvt_scalef32_pk32_f32_fp6 v[0:31], v[146:151], 1.0
	v_pk_fma_f32 v[32:33], v[48:49], v[144:145], v[32:33] op_sel_hi:[1,0,1]
	v_pk_fma_f32 v[34:35], v[50:51], v[144:145], v[34:35] op_sel_hi:[1,0,1]
	v_pk_fma_f32 v[36:37], v[52:53], v[144:145], v[36:37] op_sel_hi:[1,0,1]
	v_pk_fma_f32 v[38:39], v[54:55], v[144:145], v[38:39] op_sel_hi:[1,0,1]
	v_pk_fma_f32 v[40:41], v[56:57], v[144:145], v[40:41] op_sel_hi:[1,0,1]
	v_pk_fma_f32 v[42:43], v[58:59], v[144:145], v[42:43] op_sel_hi:[1,0,1]
	v_pk_fma_f32 v[44:45], v[60:61], v[144:145], v[44:45] op_sel_hi:[1,0,1]
	v_pk_fma_f32 v[46:47], v[62:63], v[144:145], v[46:47] op_sel_hi:[1,0,1]
	s_waitcnt vmcnt(16)
	v_lshlrev_b32_e32 v167, 16, v159
	v_lshlrev_b32_e32 v166, 16, v158
	v_and_b32_e32 v169, 0xffff0000, v159
	v_and_b32_e32 v168, 0xffff0000, v158
	s_waitcnt vmcnt(14)
	v_mov_b32_e32 v157, v220
	v_mov_b32_e32 v158, v221
	v_mov_b32_e32 v159, v222
	v_mov_b32_e32 v146, v191
	v_pk_fma_f32 v[0:1], v[0:1], v[190:191], v[32:33] op_sel_hi:[1,0,1]
	v_pk_fma_f32 v[2:3], v[2:3], v[190:191], v[34:35] op_sel_hi:[1,0,1]
	v_pk_fma_f32 v[4:5], v[4:5], v[190:191], v[36:37] op_sel_hi:[1,0,1]
	v_pk_fma_f32 v[6:7], v[6:7], v[190:191], v[38:39] op_sel_hi:[1,0,1]
	v_pk_fma_f32 v[8:9], v[8:9], v[190:191], v[40:41] op_sel_hi:[1,0,1]
	v_pk_fma_f32 v[10:11], v[10:11], v[190:191], v[42:43] op_sel_hi:[1,0,1]
	v_pk_fma_f32 v[12:13], v[12:13], v[190:191], v[44:45] op_sel_hi:[1,0,1]
	v_pk_fma_f32 v[14:15], v[14:15], v[190:191], v[46:47] op_sel_hi:[1,0,1]
	s_waitcnt vmcnt(12)
	v_mov_b32_e32 v183, v224
	v_mov_b32_e32 v184, v225
	v_mov_b32_e32 v185, v226
	s_waitcnt vmcnt(10)
	v_mov_b32_e32 v189, v228
	v_mov_b32_e32 v190, v229
	v_mov_b32_e32 v191, v230
	s_waitcnt vmcnt(8)
	v_mov_b32_e32 v195, v232
	v_mov_b32_e32 v196, v233
	v_mov_b32_e32 v197, v234
	ds_read2_b32 v[220:221], v177 offset0:32 offset1:36
	ds_read2_b32 v[222:223], v177 offset0:40 offset1:44
	ds_read2_b32 v[242:243], v177 offset0:48 offset1:52
	ds_read2_b32 v[244:245], v177 offset0:56 offset1:60
	v_cvt_scalef32_pk32_f32_fp6 v[96:127], v[154:159], 1.0
	ds_read_u16 v131, v152 offset:128
	ds_read_u16 v135, v152 offset:136
	ds_read_u16 v139, v152 offset:144
	ds_read_u16 v143, v152 offset:152
	ds_read_u16 v153, v152 offset:160
	ds_read_u16 v154, v152 offset:168
	ds_read_u16 v155, v152 offset:176
	ds_read_u16 v152, v152 offset:184
	v_pk_fma_f32 v[144:145], v[16:17], v[146:147], v[0:1] op_sel_hi:[1,0,1]
	v_pk_fma_f32 v[148:149], v[18:19], v[146:147], v[2:3] op_sel_hi:[1,0,1]
	v_pk_fma_f32 v[150:151], v[20:21], v[146:147], v[4:5] op_sel_hi:[1,0,1]
	v_pk_fma_f32 v[202:203], v[22:23], v[146:147], v[6:7] op_sel_hi:[1,0,1]
	v_pk_fma_f32 v[208:209], v[24:25], v[146:147], v[8:9] op_sel_hi:[1,0,1]
	v_pk_fma_f32 v[214:215], v[26:27], v[146:147], v[10:11] op_sel_hi:[1,0,1]
	v_pk_fma_f32 v[236:237], v[28:29], v[146:147], v[12:13] op_sel_hi:[1,0,1]
	v_pk_fma_f32 v[146:147], v[30:31], v[146:147], v[14:15] op_sel_hi:[1,0,1]
	s_waitcnt lgkmcnt(11)
	v_pk_fma_f32 v[96:97], v[96:97], v[220:221], v[144:145] op_sel_hi:[1,0,1]
	v_mov_b32_e32 v144, v221
	v_cvt_scalef32_pk32_f32_fp6 v[64:95], v[180:185], 1.0
	v_pk_fma_f32 v[98:99], v[98:99], v[220:221], v[148:149] op_sel_hi:[1,0,1]
	v_pk_fma_f32 v[100:101], v[100:101], v[220:221], v[150:151] op_sel_hi:[1,0,1]
	v_pk_fma_f32 v[102:103], v[102:103], v[220:221], v[202:203] op_sel_hi:[1,0,1]
	v_pk_fma_f32 v[104:105], v[104:105], v[220:221], v[208:209] op_sel_hi:[1,0,1]
	v_pk_fma_f32 v[106:107], v[106:107], v[220:221], v[214:215] op_sel_hi:[1,0,1]
	v_pk_fma_f32 v[108:109], v[108:109], v[220:221], v[236:237] op_sel_hi:[1,0,1]
	v_pk_fma_f32 v[110:111], v[110:111], v[220:221], v[146:147] op_sel_hi:[1,0,1]
	v_pk_fma_f32 v[96:97], v[112:113], v[144:145], v[96:97] op_sel_hi:[1,0,1]
	s_waitcnt lgkmcnt(7)
	v_add_u32_e32 v112, s21, v131
	v_pk_fma_f32 v[98:99], v[114:115], v[144:145], v[98:99] op_sel_hi:[1,0,1]
	v_pk_fma_f32 v[100:101], v[116:117], v[144:145], v[100:101] op_sel_hi:[1,0,1]
	v_pk_fma_f32 v[102:103], v[118:119], v[144:145], v[102:103] op_sel_hi:[1,0,1]
	v_pk_fma_f32 v[104:105], v[120:121], v[144:145], v[104:105] op_sel_hi:[1,0,1]
	v_pk_fma_f32 v[106:107], v[122:123], v[144:145], v[106:107] op_sel_hi:[1,0,1]
	v_pk_fma_f32 v[108:109], v[124:125], v[144:145], v[108:109] op_sel_hi:[1,0,1]
	v_pk_fma_f32 v[110:111], v[126:127], v[144:145], v[110:111] op_sel_hi:[1,0,1]
	s_waitcnt lgkmcnt(6)
	v_add_u32_e32 v113, s21, v135
	s_waitcnt lgkmcnt(5)
	v_add_u32_e32 v114, s21, v139
	s_waitcnt lgkmcnt(4)
	v_add_u32_e32 v115, s21, v143
	s_waitcnt lgkmcnt(3)
	v_add_u32_e32 v116, s21, v153
	s_waitcnt lgkmcnt(2)
; #define P12_VISSUE(c_, i_, q_, D_X) do { _Pragma("unroll") for (int b = 0; b < 8; ++b) { const int idx = ((q_) * 8 + b) * 4 + eg; const unsigned ro = (unsigned)(c_) * 16384u + (unsigned)EL[(i_) * 128 + idx]; \
;           const v3u_ ld_ = *(const v3u_*)(V8 + (size_t)(ro * 192u + 12u * (unsigned)cl)); if (b & 1) D_X[b >> 1].hi = ld_; else D_X[b >> 1].lo = ld_; } } while (0)
; __device__ __forceinline__ void p12_peer(Frame& F) {
;     ...
;       v6u_ dA[4], dB[4];
;       P12_VISSUE(0, 0, 0, dA);
; _Pragma("nounroll")
;       for (int c = 0; c < 16; ++c) {
;           int lo_ = 16 * cl + 4 * eg; asm volatile("" : "+v"(lo_));
; _Pragma("nounroll")
;           for (int i = 0; i < 4; ++i) { const int t = F.gw + i * F.NGW;
;               f32x2 acc2[8];
; #pragma unroll
;               for (int m = 0; m < 8; ++m) acc2[m] = (f32x2){0.f, 0.f};
;               const v2u hb = *(const v2u*)(HN + ((size_t)t * D_ + (size_t)(unsigned)(256 * c + lo_)));
;               P12_VISSUE(c, i, 1, dB); asm volatile("" ::: "memory"); P12_VCOMP(i, 0, dA);
;               P12_VISSUE(c, i, 2, dA); asm volatile("" ::: "memory"); P12_VCOMP(i, 1, dB);
;               P12_VISSUE(c, i, 3, dB); asm volatile("" ::: "memory"); P12_VCOMP(i, 2, dA);
;               { const int in_ = i + 1 < 4 ? i + 1 : 0, cn_ = i + 1 < 4 ? c : (c + 1 < 16 ? c + 1 : 15); P12_VISSUE(cn_, in_, 0, dA); } asm volatile("" ::: "memory"); P12_VCOMP(i, 3, dB);
	v_add_u32_e32 v117, s21, v154
	s_waitcnt lgkmcnt(1)
	v_add_u32_e32 v118, s21, v155
	s_waitcnt lgkmcnt(0)
	v_add_u32_e32 v119, s21, v152
	v_pk_fma_f32 v[64:65], v[64:65], v[222:223], v[96:97] op_sel_hi:[1,0,1]
	v_mad_u64_u32 v[96:97], s[30:31], v112, s16, v[160:161]
	v_cvt_scalef32_pk32_f32_fp6 v[32:63], v[186:191], 1.0
	v_cvt_scalef32_pk32_f32_fp6 v[0:31], v[192:197], 1.0
	v_mov_b32_e32 v146, v223
	v_pk_fma_f32 v[66:67], v[66:67], v[222:223], v[98:99] op_sel_hi:[1,0,1]
	v_pk_fma_f32 v[68:69], v[68:69], v[222:223], v[100:101] op_sel_hi:[1,0,1]
	v_pk_fma_f32 v[70:71], v[70:71], v[222:223], v[102:103] op_sel_hi:[1,0,1]
	v_pk_fma_f32 v[72:73], v[72:73], v[222:223], v[104:105] op_sel_hi:[1,0,1]
	v_pk_fma_f32 v[74:75], v[74:75], v[222:223], v[106:107] op_sel_hi:[1,0,1]
	v_pk_fma_f32 v[76:77], v[76:77], v[222:223], v[108:109] op_sel_hi:[1,0,1]
	v_pk_fma_f32 v[78:79], v[78:79], v[222:223], v[110:111] op_sel_hi:[1,0,1]
	v_mad_u64_u32 v[98:99], s[30:31], v113, s16, v[160:161]
	v_mad_u64_u32 v[100:101], s[30:31], v114, s16, v[160:161]
	v_mad_u64_u32 v[102:103], s[30:31], v115, s16, v[160:161]
	v_mad_u64_u32 v[104:105], s[30:31], v116, s16, v[160:161]
	v_mad_u64_u32 v[106:107], s[30:31], v117, s16, v[160:161]
	v_mad_u64_u32 v[108:109], s[30:31], v118, s16, v[160:161]
	v_mad_u64_u32 v[110:111], s[30:31], v119, s16, v[160:161]
	global_load_dwordx3 v[180:182], v96, s[2:3]
	global_load_dwordx3 v[226:228], v98, s[2:3]
	global_load_dwordx3 v[186:188], v100, s[2:3]
	global_load_dwordx3 v[230:232], v102, s[2:3]
	global_load_dwordx3 v[192:194], v104, s[2:3]
	global_load_dwordx3 v[234:236], v106, s[2:3]
	global_load_dwordx3 v[222:224], v108, s[2:3]
	global_load_dwordx3 v[238:240], v110, s[2:3]
	s_waitcnt vmcnt(14)
	v_mov_b32_e32 v201, v128
	v_mov_b32_e32 v202, v129
	v_mov_b32_e32 v203, v130
	s_waitcnt vmcnt(12)
	v_mov_b32_e32 v207, v132
	v_mov_b32_e32 v208, v133
	v_mov_b32_e32 v209, v134
	s_waitcnt vmcnt(10)
	v_mov_b32_e32 v213, v136
	v_mov_b32_e32 v214, v137
	v_mov_b32_e32 v215, v138
	s_waitcnt vmcnt(8)
	v_mov_b32_e32 v219, v140
	v_mov_b32_e32 v220, v141
	v_mov_b32_e32 v221, v142
	v_pk_fma_f32 v[64:65], v[80:81], v[146:147], v[64:65] op_sel_hi:[1,0,1]
	v_pk_fma_f32 v[66:67], v[82:83], v[146:147], v[66:67] op_sel_hi:[1,0,1]
	v_pk_fma_f32 v[68:69], v[84:85], v[146:147], v[68:69] op_sel_hi:[1,0,1]
	v_pk_fma_f32 v[70:71], v[86:87], v[146:147], v[70:71] op_sel_hi:[1,0,1]
	v_pk_fma_f32 v[72:73], v[88:89], v[146:147], v[72:73] op_sel_hi:[1,0,1]
	v_pk_fma_f32 v[74:75], v[90:91], v[146:147], v[74:75] op_sel_hi:[1,0,1]
	v_pk_fma_f32 v[76:77], v[92:93], v[146:147], v[76:77] op_sel_hi:[1,0,1]
	v_pk_fma_f32 v[78:79], v[94:95], v[146:147], v[78:79] op_sel_hi:[1,0,1]
	ds_read2_b32 v[196:197], v177 offset0:64 offset1:68
	v_mov_b32_e32 v184, v243
	ds_read2_b32 v[246:247], v177 offset0:72 offset1:76
	ds_read2_b32 v[248:249], v177 offset0:80 offset1:84
	ds_read2_b32 v[250:251], v177 offset0:88 offset1:92
	v_pk_fma_f32 v[32:33], v[32:33], v[242:243], v[64:65] op_sel_hi:[1,0,1]
	v_pk_fma_f32 v[34:35], v[34:35], v[242:243], v[66:67] op_sel_hi:[1,0,1]
	v_pk_fma_f32 v[36:37], v[36:37], v[242:243], v[68:69] op_sel_hi:[1,0,1]
	v_pk_fma_f32 v[38:39], v[38:39], v[242:243], v[70:71] op_sel_hi:[1,0,1]
	v_pk_fma_f32 v[40:41], v[40:41], v[242:243], v[72:73] op_sel_hi:[1,0,1]
	v_pk_fma_f32 v[42:43], v[42:43], v[242:243], v[74:75] op_sel_hi:[1,0,1]
	v_pk_fma_f32 v[44:45], v[44:45], v[242:243], v[76:77] op_sel_hi:[1,0,1]
	v_pk_fma_f32 v[46:47], v[46:47], v[242:243], v[78:79] op_sel_hi:[1,0,1]
	v_cvt_scalef32_pk32_f32_fp6 v[128:159], v[198:203], 1.0
	v_cvt_scalef32_pk32_f32_fp6 v[96:127], v[204:209], 1.0
	v_cvt_scalef32_pk32_f32_fp6 v[64:95], v[210:215], 1.0
	v_pk_fma_f32 v[198:199], v[48:49], v[184:185], v[32:33] op_sel_hi:[1,0,1]
	v_pk_fma_f32 v[200:201], v[50:51], v[184:185], v[34:35] op_sel_hi:[1,0,1]
	v_pk_fma_f32 v[202:203], v[52:53], v[184:185], v[36:37] op_sel_hi:[1,0,1]
	v_pk_fma_f32 v[204:205], v[54:55], v[184:185], v[38:39] op_sel_hi:[1,0,1]
	v_pk_fma_f32 v[206:207], v[56:57], v[184:185], v[40:41] op_sel_hi:[1,0,1]
	v_pk_fma_f32 v[208:209], v[58:59], v[184:185], v[42:43] op_sel_hi:[1,0,1]
	v_pk_fma_f32 v[210:211], v[60:61], v[184:185], v[44:45] op_sel_hi:[1,0,1]
	v_pk_fma_f32 v[184:185], v[62:63], v[184:185], v[46:47] op_sel_hi:[1,0,1]
	ds_read_u16 v183, v179 offset:16384
	ds_read_u16 v189, v179 offset:16392
	ds_read_u16 v191, v179 offset:16400
	ds_read_u16 v195, v179 offset:16408
	ds_read_u16 v212, v179 offset:16416
	ds_read_u16 v213, v179 offset:16424
	ds_read_u16 v214, v179 offset:16432
	ds_read_u16 v179, v179 offset:16440
	v_mov_b32_e32 v190, v245
	v_pk_fma_f32 v[0:1], v[0:1], v[244:245], v[198:199] op_sel_hi:[1,0,1]
	v_pk_fma_f32 v[2:3], v[2:3], v[244:245], v[200:201] op_sel_hi:[1,0,1]
	v_pk_fma_f32 v[4:5], v[4:5], v[244:245], v[202:203] op_sel_hi:[1,0,1]
	v_pk_fma_f32 v[6:7], v[6:7], v[244:245], v[204:205] op_sel_hi:[1,0,1]
	v_pk_fma_f32 v[8:9], v[8:9], v[244:245], v[206:207] op_sel_hi:[1,0,1]
	v_pk_fma_f32 v[10:11], v[10:11], v[244:245], v[208:209] op_sel_hi:[1,0,1]
	v_pk_fma_f32 v[12:13], v[12:13], v[244:245], v[210:211] op_sel_hi:[1,0,1]
	v_pk_fma_f32 v[14:15], v[14:15], v[244:245], v[184:185] op_sel_hi:[1,0,1]
	s_cselect_b32 s29, s22, s17
	s_waitcnt lgkmcnt(5)
; #define P12_VISSUE(c_, i_, q_, D_X) do { _Pragma("unroll") for (int b = 0; b < 8; ++b) { const int idx = ((q_) * 8 + b) * 4 + eg; const unsigned ro = (unsigned)(c_) * 16384u + (unsigned)EL[(i_) * 128 + idx]; \
;           const v3u_ ld_ = *(const v3u_*)(V8 + (size_t)(ro * 192u + 12u * (unsigned)cl)); if (b & 1) D_X[b >> 1].hi = ld_; else D_X[b >> 1].lo = ld_; } } while (0)
; __device__ __forceinline__ void p12_peer(Frame& F) {
;     ...
;       v6u_ dA[4], dB[4];
;       P12_VISSUE(0, 0, 0, dA);
; _Pragma("nounroll")
;       for (int c = 0; c < 16; ++c) {
;           int lo_ = 16 * cl + 4 * eg; asm volatile("" : "+v"(lo_));
; _Pragma("nounroll")
;           for (int i = 0; i < 4; ++i) { const int t = F.gw + i * F.NGW;
;               f32x2 acc2[8];
; #pragma unroll
;               for (int m = 0; m < 8; ++m) acc2[m] = (f32x2){0.f, 0.f};
;               const v2u hb = *(const v2u*)(HN + ((size_t)t * D_ + (size_t)(unsigned)(256 * c + lo_)));
;               P12_VISSUE(c, i, 1, dB); asm volatile("" ::: "memory"); P12_VCOMP(i, 0, dA);
;               P12_VISSUE(c, i, 2, dA); asm volatile("" ::: "memory"); P12_VCOMP(i, 1, dB);
;               P12_VISSUE(c, i, 3, dB); asm volatile("" ::: "memory"); P12_VCOMP(i, 2, dA);
;               { const int in_ = i + 1 < 4 ? i + 1 : 0, cn_ = i + 1 < 4 ? c : (c + 1 < 16 ? c + 1 : 15); P12_VISSUE(cn_, in_, 0, dA); } asm volatile("" ::: "memory"); P12_VCOMP(i, 3, dB);
	v_pk_fma_f32 v[0:1], v[16:17], v[190:191], v[0:1] op_sel_hi:[1,0,1]
	v_pk_fma_f32 v[2:3], v[18:19], v[190:191], v[2:3] op_sel_hi:[1,0,1]
	v_pk_fma_f32 v[4:5], v[20:21], v[190:191], v[4:5] op_sel_hi:[1,0,1]
	v_pk_fma_f32 v[6:7], v[22:23], v[190:191], v[6:7] op_sel_hi:[1,0,1]
	v_pk_fma_f32 v[8:9], v[24:25], v[190:191], v[8:9] op_sel_hi:[1,0,1]
	v_pk_fma_f32 v[10:11], v[26:27], v[190:191], v[10:11] op_sel_hi:[1,0,1]
	v_pk_fma_f32 v[12:13], v[28:29], v[190:191], v[12:13] op_sel_hi:[1,0,1]
	v_pk_fma_f32 v[14:15], v[30:31], v[190:191], v[14:15] op_sel_hi:[1,0,1]
	s_lshl_b64 s[14:15], s[12:13], 14
	s_lshl_b32 s13, s29, 14
	v_pk_fma_f32 v[0:1], v[128:129], v[196:197], v[0:1] op_sel_hi:[1,0,1]
	v_pk_fma_f32 v[2:3], v[130:131], v[196:197], v[2:3] op_sel_hi:[1,0,1]
	v_pk_fma_f32 v[4:5], v[132:133], v[196:197], v[4:5] op_sel_hi:[1,0,1]
	v_pk_fma_f32 v[6:7], v[134:135], v[196:197], v[6:7] op_sel_hi:[1,0,1]
	v_pk_fma_f32 v[8:9], v[136:137], v[196:197], v[8:9] op_sel_hi:[1,0,1]
	v_pk_fma_f32 v[10:11], v[138:139], v[196:197], v[10:11] op_sel_hi:[1,0,1]
	v_pk_fma_f32 v[12:13], v[140:141], v[196:197], v[12:13] op_sel_hi:[1,0,1]
	v_pk_fma_f32 v[14:15], v[142:143], v[196:197], v[14:15] op_sel_hi:[1,0,1]
	v_mov_b32_e32 v16, v197
	v_pk_fma_f32 v[0:1], v[144:145], v[16:17], v[0:1] op_sel_hi:[1,0,1]
	v_pk_fma_f32 v[2:3], v[146:147], v[16:17], v[2:3] op_sel_hi:[1,0,1]
	v_pk_fma_f32 v[4:5], v[148:149], v[16:17], v[4:5] op_sel_hi:[1,0,1]
	v_pk_fma_f32 v[6:7], v[150:151], v[16:17], v[6:7] op_sel_hi:[1,0,1]
	v_pk_fma_f32 v[8:9], v[152:153], v[16:17], v[8:9] op_sel_hi:[1,0,1]
	v_pk_fma_f32 v[10:11], v[154:155], v[16:17], v[10:11] op_sel_hi:[1,0,1]
	v_pk_fma_f32 v[12:13], v[156:157], v[16:17], v[12:13] op_sel_hi:[1,0,1]
	v_pk_fma_f32 v[14:15], v[158:159], v[16:17], v[14:15] op_sel_hi:[1,0,1]
	v_add_u32_e32 v16, s13, v183
	v_add_u32_e32 v19, s13, v189
	v_add_u32_e32 v21, s13, v191
	s_waitcnt lgkmcnt(4)
	v_add_u32_e32 v23, s13, v195
	s_waitcnt lgkmcnt(3)
	v_add_u32_e32 v30, s13, v212
	s_waitcnt lgkmcnt(2)
	v_add_u32_e32 v128, s13, v213
	s_waitcnt lgkmcnt(1)
	v_add_u32_e32 v129, s13, v214
	s_waitcnt lgkmcnt(0)
	v_add_u32_e32 v130, s13, v179
	v_mad_u64_u32 v[16:17], s[30:31], v16, s16, v[160:161]
	v_pk_fma_f32 v[0:1], v[96:97], v[246:247], v[0:1] op_sel_hi:[1,0,1]
	v_pk_fma_f32 v[2:3], v[98:99], v[246:247], v[2:3] op_sel_hi:[1,0,1]
	v_pk_fma_f32 v[4:5], v[100:101], v[246:247], v[4:5] op_sel_hi:[1,0,1]
	v_mad_u64_u32 v[24:25], s[30:31], v19, s16, v[160:161]
	v_mad_u64_u32 v[26:27], s[30:31], v21, s16, v[160:161]
	v_mad_u64_u32 v[28:29], s[30:31], v23, s16, v[160:161]
	v_mad_u64_u32 v[30:31], s[30:31], v30, s16, v[160:161]
	v_mad_u64_u32 v[96:97], s[30:31], v128, s16, v[160:161]
	v_mad_u64_u32 v[98:99], s[30:31], v129, s16, v[160:161]
	v_mad_u64_u32 v[100:101], s[30:31], v130, s16, v[160:161]
	global_load_dwordx3 v[134:136], v16, s[2:3]
	global_load_dwordx3 v[152:154], v24, s[2:3]
	global_load_dwordx3 v[128:130], v26, s[2:3]
	global_load_dwordx3 v[156:158], v28, s[2:3]
	global_load_dwordx3 v[140:142], v30, s[2:3]
	global_load_dwordx3 v[198:200], v96, s[2:3]
	global_load_dwordx3 v[146:148], v98, s[2:3]
	global_load_dwordx3 v[202:204], v100, s[2:3]
	v_mov_b32_e32 v18, v247
	v_pk_fma_f32 v[6:7], v[102:103], v[246:247], v[6:7] op_sel_hi:[1,0,1]
	v_pk_fma_f32 v[8:9], v[104:105], v[246:247], v[8:9] op_sel_hi:[1,0,1]
	v_pk_fma_f32 v[10:11], v[106:107], v[246:247], v[10:11] op_sel_hi:[1,0,1]
	v_pk_fma_f32 v[12:13], v[108:109], v[246:247], v[12:13] op_sel_hi:[1,0,1]
	v_pk_fma_f32 v[14:15], v[110:111], v[246:247], v[14:15] op_sel_hi:[1,0,1]
	s_waitcnt vmcnt(14)
	v_mov_b32_e32 v183, v226
	v_mov_b32_e32 v184, v227
	v_mov_b32_e32 v185, v228
	v_pk_fma_f32 v[0:1], v[112:113], v[18:19], v[0:1] op_sel_hi:[1,0,1]
	v_pk_fma_f32 v[2:3], v[114:115], v[18:19], v[2:3] op_sel_hi:[1,0,1]
	v_pk_fma_f32 v[4:5], v[116:117], v[18:19], v[4:5] op_sel_hi:[1,0,1]
	v_pk_fma_f32 v[6:7], v[118:119], v[18:19], v[6:7] op_sel_hi:[1,0,1]
	v_pk_fma_f32 v[8:9], v[120:121], v[18:19], v[8:9] op_sel_hi:[1,0,1]
	v_pk_fma_f32 v[10:11], v[122:123], v[18:19], v[10:11] op_sel_hi:[1,0,1]
	v_pk_fma_f32 v[12:13], v[124:125], v[18:19], v[12:13] op_sel_hi:[1,0,1]
	v_pk_fma_f32 v[14:15], v[126:127], v[18:19], v[14:15] op_sel_hi:[1,0,1]
	ds_read2_b32 v[214:215], v177 offset0:96 offset1:100
	v_mov_b32_e32 v20, v249
	v_pk_fma_f32 v[0:1], v[64:65], v[248:249], v[0:1] op_sel_hi:[1,0,1]
	v_pk_fma_f32 v[2:3], v[66:67], v[248:249], v[2:3] op_sel_hi:[1,0,1]
	v_pk_fma_f32 v[4:5], v[68:69], v[248:249], v[4:5] op_sel_hi:[1,0,1]
	v_pk_fma_f32 v[6:7], v[70:71], v[248:249], v[6:7] op_sel_hi:[1,0,1]
	v_pk_fma_f32 v[8:9], v[72:73], v[248:249], v[8:9] op_sel_hi:[1,0,1]
	v_pk_fma_f32 v[10:11], v[74:75], v[248:249], v[10:11] op_sel_hi:[1,0,1]
	v_pk_fma_f32 v[12:13], v[76:77], v[248:249], v[12:13] op_sel_hi:[1,0,1]
	v_pk_fma_f32 v[14:15], v[78:79], v[248:249], v[14:15] op_sel_hi:[1,0,1]
	s_waitcnt vmcnt(12)
	v_mov_b32_e32 v189, v230
	v_mov_b32_e32 v190, v231
	v_mov_b32_e32 v191, v232
	v_cvt_scalef32_pk32_f32_fp6 v[32:63], v[216:221], 1.0
	v_pk_fma_f32 v[0:1], v[80:81], v[20:21], v[0:1] op_sel_hi:[1,0,1]
	v_pk_fma_f32 v[2:3], v[82:83], v[20:21], v[2:3] op_sel_hi:[1,0,1]
	v_pk_fma_f32 v[4:5], v[84:85], v[20:21], v[4:5] op_sel_hi:[1,0,1]
	v_pk_fma_f32 v[6:7], v[86:87], v[20:21], v[6:7] op_sel_hi:[1,0,1]
	v_pk_fma_f32 v[8:9], v[88:89], v[20:21], v[8:9] op_sel_hi:[1,0,1]
	v_pk_fma_f32 v[10:11], v[90:91], v[20:21], v[10:11] op_sel_hi:[1,0,1]
	v_pk_fma_f32 v[12:13], v[92:93], v[20:21], v[12:13] op_sel_hi:[1,0,1]
	v_pk_fma_f32 v[14:15], v[94:95], v[20:21], v[14:15] op_sel_hi:[1,0,1]
	ds_read2_b32 v[216:217], v177 offset0:104 offset1:108
	v_mov_b32_e32 v22, v251
	v_pk_fma_f32 v[0:1], v[32:33], v[250:251], v[0:1] op_sel_hi:[1,0,1]
	v_pk_fma_f32 v[2:3], v[34:35], v[250:251], v[2:3] op_sel_hi:[1,0,1]
	v_pk_fma_f32 v[4:5], v[36:37], v[250:251], v[4:5] op_sel_hi:[1,0,1]
	v_pk_fma_f32 v[6:7], v[38:39], v[250:251], v[6:7] op_sel_hi:[1,0,1]
	v_pk_fma_f32 v[8:9], v[40:41], v[250:251], v[8:9] op_sel_hi:[1,0,1]
	v_pk_fma_f32 v[10:11], v[42:43], v[250:251], v[10:11] op_sel_hi:[1,0,1]
	v_pk_fma_f32 v[12:13], v[44:45], v[250:251], v[12:13] op_sel_hi:[1,0,1]
	v_pk_fma_f32 v[14:15], v[46:47], v[250:251], v[14:15] op_sel_hi:[1,0,1]
	s_waitcnt vmcnt(10)
; #define P12_VISSUE(c_, i_, q_, D_X) do { _Pragma("unroll") for (int b = 0; b < 8; ++b) { const int idx = ((q_) * 8 + b) * 4 + eg; const unsigned ro = (unsigned)(c_) * 16384u + (unsigned)EL[(i_) * 128 + idx]; \
;           const v3u_ ld_ = *(const v3u_*)(V8 + (size_t)(ro * 192u + 12u * (unsigned)cl)); if (b & 1) D_X[b >> 1].hi = ld_; else D_X[b >> 1].lo = ld_; } } while (0)
; __device__ __forceinline__ void p12_peer(Frame& F) {
;     ...
;       v6u_ dA[4], dB[4];
;       P12_VISSUE(0, 0, 0, dA);
; _Pragma("nounroll")
;       for (int c = 0; c < 16; ++c) {
;           int lo_ = 16 * cl + 4 * eg; asm volatile("" : "+v"(lo_));
; _Pragma("nounroll")
;           for (int i = 0; i < 4; ++i) { const int t = F.gw + i * F.NGW;
;               f32x2 acc2[8];
; #pragma unroll
;               for (int m = 0; m < 8; ++m) acc2[m] = (f32x2){0.f, 0.f};
;               const v2u hb = *(const v2u*)(HN + ((size_t)t * D_ + (size_t)(unsigned)(256 * c + lo_)));
;               P12_VISSUE(c, i, 1, dB); asm volatile("" ::: "memory"); P12_VCOMP(i, 0, dA);
;               P12_VISSUE(c, i, 2, dA); asm volatile("" ::: "memory"); P12_VCOMP(i, 1, dB);
;               P12_VISSUE(c, i, 3, dB); asm volatile("" ::: "memory"); P12_VCOMP(i, 2, dA);
;               { const int in_ = i + 1 < 4 ? i + 1 : 0, cn_ = i + 1 < 4 ? c : (c + 1 < 16 ? c + 1 : 15); P12_VISSUE(cn_, in_, 0, dA); } asm volatile("" ::: "memory"); P12_VCOMP(i, 3, dB);
;               float r8[8], r4[4];
; #pragma unroll
;               for (int m = 0; m < 8; ++m) { const float lo_v = (m & 1) ? acc2[m >> 1].y : acc2[m >> 1].x, hi_v = (m & 1) ? acc2[4 + (m >> 1)].y : acc2[4 + (m >> 1)].x;
;                   const float keep = hi5 ? hi_v : lo_v, send = hi5 ? lo_v : hi_v;
;                   r8[m] = keep + __builtin_bit_cast(float, __builtin_amdgcn_ds_bpermute((F.lane ^ 32) << 2, __builtin_bit_cast(int, send))); }
; #pragma unroll
;               for (int m = 0; m < 4; ++m) { const float keep = hi4 ? r8[4 + m] : r8[m], send = hi4 ? r8[m] : r8[4 + m];
;                   r4[m] = keep + __builtin_bit_cast(float, __builtin_amdgcn_ds_bpermute((F.lane ^ 16) << 2, __builtin_bit_cast(int, send))); }
;               int lo3_ = lo_; asm volatile("" : "+v"(lo3_));
;               const size_t col = (size_t)t * D_ + (size_t)(unsigned)(256 * c + lo3_);
	v_mov_b32_e32 v195, v234
	v_mov_b32_e32 v196, v235
	v_mov_b32_e32 v197, v236
	v_mov_b32_e32 v162, v176
	v_pk_fma_f32 v[132:133], v[48:49], v[22:23], v[0:1] op_sel_hi:[1,0,1]
	v_pk_fma_f32 v[138:139], v[50:51], v[22:23], v[2:3] op_sel_hi:[1,0,1]
	v_pk_fma_f32 v[144:145], v[52:53], v[22:23], v[4:5] op_sel_hi:[1,0,1]
	v_pk_fma_f32 v[150:151], v[54:55], v[22:23], v[6:7] op_sel_hi:[1,0,1]
	v_pk_fma_f32 v[206:207], v[56:57], v[22:23], v[8:9] op_sel_hi:[1,0,1]
	v_pk_fma_f32 v[208:209], v[58:59], v[22:23], v[10:11] op_sel_hi:[1,0,1]
	v_pk_fma_f32 v[210:211], v[60:61], v[22:23], v[12:13] op_sel_hi:[1,0,1]
	v_pk_fma_f32 v[212:213], v[62:63], v[22:23], v[14:15] op_sel_hi:[1,0,1]
	s_waitcnt vmcnt(8)
	v_mov_b32_e32 v225, v238
	v_mov_b32_e32 v226, v239
	v_mov_b32_e32 v227, v240
	ds_read2_b32 v[218:219], v177 offset0:112 offset1:116
	v_cvt_scalef32_pk32_f32_fp6 v[96:127], v[180:185], 1.0
	s_add_u32 s14, s26, s14
	ds_read2_b32 v[220:221], v177 offset0:120 offset1:124
	s_waitcnt lgkmcnt(3)
	v_pk_fma_f32 v[96:97], v[96:97], v[214:215], v[132:133] op_sel_hi:[1,0,1]
	v_pk_fma_f32 v[98:99], v[98:99], v[214:215], v[138:139] op_sel_hi:[1,0,1]
	v_pk_fma_f32 v[100:101], v[100:101], v[214:215], v[144:145] op_sel_hi:[1,0,1]
	v_pk_fma_f32 v[102:103], v[102:103], v[214:215], v[150:151] op_sel_hi:[1,0,1]
	v_pk_fma_f32 v[104:105], v[104:105], v[214:215], v[206:207] op_sel_hi:[1,0,1]
	v_pk_fma_f32 v[106:107], v[106:107], v[214:215], v[208:209] op_sel_hi:[1,0,1]
	v_pk_fma_f32 v[108:109], v[108:109], v[214:215], v[210:211] op_sel_hi:[1,0,1]
	v_pk_fma_f32 v[110:111], v[110:111], v[214:215], v[212:213] op_sel_hi:[1,0,1]
	v_mov_b32_e32 v132, v215
	s_addc_u32 s15, s27, s15
	v_cvt_scalef32_pk32_f32_fp6 v[64:95], v[186:191], 1.0
	v_add_u32_e32 v162, s18, v162
	v_pk_fma_f32 v[96:97], v[112:113], v[132:133], v[96:97] op_sel_hi:[1,0,1]
	v_pk_fma_f32 v[98:99], v[114:115], v[132:133], v[98:99] op_sel_hi:[1,0,1]
	v_pk_fma_f32 v[100:101], v[116:117], v[132:133], v[100:101] op_sel_hi:[1,0,1]
	v_pk_fma_f32 v[102:103], v[118:119], v[132:133], v[102:103] op_sel_hi:[1,0,1]
	v_pk_fma_f32 v[104:105], v[120:121], v[132:133], v[104:105] op_sel_hi:[1,0,1]
	v_pk_fma_f32 v[106:107], v[122:123], v[132:133], v[106:107] op_sel_hi:[1,0,1]
	v_pk_fma_f32 v[108:109], v[124:125], v[132:133], v[108:109] op_sel_hi:[1,0,1]
	v_pk_fma_f32 v[110:111], v[126:127], v[132:133], v[110:111] op_sel_hi:[1,0,1]
	v_lshl_add_u64 v[180:181], v[162:163], 2, s[14:15]
	s_waitcnt lgkmcnt(2)
	v_mov_b32_e32 v162, v217
	v_pk_fma_f32 v[64:65], v[64:65], v[216:217], v[96:97] op_sel_hi:[1,0,1]
	v_pk_fma_f32 v[66:67], v[66:67], v[216:217], v[98:99] op_sel_hi:[1,0,1]
	v_pk_fma_f32 v[68:69], v[68:69], v[216:217], v[100:101] op_sel_hi:[1,0,1]
	v_pk_fma_f32 v[70:71], v[70:71], v[216:217], v[102:103] op_sel_hi:[1,0,1]
	v_pk_fma_f32 v[72:73], v[72:73], v[216:217], v[104:105] op_sel_hi:[1,0,1]
	v_pk_fma_f32 v[74:75], v[74:75], v[216:217], v[106:107] op_sel_hi:[1,0,1]
	v_pk_fma_f32 v[76:77], v[76:77], v[216:217], v[108:109] op_sel_hi:[1,0,1]
	v_pk_fma_f32 v[78:79], v[78:79], v[216:217], v[110:111] op_sel_hi:[1,0,1]
	v_cvt_scalef32_pk32_f32_fp6 v[32:63], v[192:197], 1.0
	v_pk_fma_f32 v[64:65], v[80:81], v[162:163], v[64:65] op_sel_hi:[1,0,1]
	v_pk_fma_f32 v[66:67], v[82:83], v[162:163], v[66:67] op_sel_hi:[1,0,1]
	v_pk_fma_f32 v[68:69], v[84:85], v[162:163], v[68:69] op_sel_hi:[1,0,1]
	v_pk_fma_f32 v[70:71], v[86:87], v[162:163], v[70:71] op_sel_hi:[1,0,1]
	v_pk_fma_f32 v[72:73], v[88:89], v[162:163], v[72:73] op_sel_hi:[1,0,1]
	v_pk_fma_f32 v[74:75], v[90:91], v[162:163], v[74:75] op_sel_hi:[1,0,1]
	v_pk_fma_f32 v[76:77], v[92:93], v[162:163], v[76:77] op_sel_hi:[1,0,1]
	v_pk_fma_f32 v[78:79], v[94:95], v[162:163], v[78:79] op_sel_hi:[1,0,1]
	s_waitcnt lgkmcnt(1)
	v_mov_b32_e32 v182, v219
	v_pk_fma_f32 v[32:33], v[32:33], v[218:219], v[64:65] op_sel_hi:[1,0,1]
	v_pk_fma_f32 v[34:35], v[34:35], v[218:219], v[66:67] op_sel_hi:[1,0,1]
	v_pk_fma_f32 v[36:37], v[36:37], v[218:219], v[68:69] op_sel_hi:[1,0,1]
	v_pk_fma_f32 v[38:39], v[38:39], v[218:219], v[70:71] op_sel_hi:[1,0,1]
	v_pk_fma_f32 v[40:41], v[40:41], v[218:219], v[72:73] op_sel_hi:[1,0,1]
	v_pk_fma_f32 v[42:43], v[42:43], v[218:219], v[74:75] op_sel_hi:[1,0,1]
	v_pk_fma_f32 v[44:45], v[44:45], v[218:219], v[76:77] op_sel_hi:[1,0,1]
	v_pk_fma_f32 v[46:47], v[46:47], v[218:219], v[78:79] op_sel_hi:[1,0,1]
	v_cvt_scalef32_pk32_f32_fp6 v[0:31], v[222:227], 1.0
	v_pk_fma_f32 v[32:33], v[48:49], v[182:183], v[32:33] op_sel_hi:[1,0,1]
	v_pk_fma_f32 v[34:35], v[50:51], v[182:183], v[34:35] op_sel_hi:[1,0,1]
	v_pk_fma_f32 v[36:37], v[52:53], v[182:183], v[36:37] op_sel_hi:[1,0,1]
	v_pk_fma_f32 v[38:39], v[54:55], v[182:183], v[38:39] op_sel_hi:[1,0,1]
	v_pk_fma_f32 v[40:41], v[56:57], v[182:183], v[40:41] op_sel_hi:[1,0,1]
	v_pk_fma_f32 v[42:43], v[58:59], v[182:183], v[42:43] op_sel_hi:[1,0,1]
	v_pk_fma_f32 v[44:45], v[60:61], v[182:183], v[44:45] op_sel_hi:[1,0,1]
	v_pk_fma_f32 v[46:47], v[62:63], v[182:183], v[46:47] op_sel_hi:[1,0,1]
	s_waitcnt lgkmcnt(0)
; __device__ __forceinline__ int fresh_lane() { int l; asm volatile("v_mbcnt_lo_u32_b32 %0, -1, 0\n\tv_mbcnt_hi_u32_b32 %0, -1, %0" : "=v"(l)); return l; }
; __device__ __forceinline__ float bflo(unsigned w) { return __uint_as_float(w << 16); }
; __device__ __forceinline__ float bfhi(unsigned w) { return __uint_as_float(w & 0xffff0000u); }
; __device__ __forceinline__ float wave_sum(float v) { v = dpp_add16(v); return (rdlane(v, 0) + rdlane(v, 16)) + (rdlane(v, 32) + rdlane(v, 48)); }
; __device__ __forceinline__ void p12_peer(Frame& F) {
;     ...
;               float r8[8], r4[4];
; #pragma unroll
;               for (int m = 0; m < 8; ++m) { const float lo_v = (m & 1) ? acc2[m >> 1].y : acc2[m >> 1].x, hi_v = (m & 1) ? acc2[4 + (m >> 1)].y : acc2[4 + (m >> 1)].x;
;                   const float keep = hi5 ? hi_v : lo_v, send = hi5 ? lo_v : hi_v;
;                   r8[m] = keep + __builtin_bit_cast(float, __builtin_amdgcn_ds_bpermute((F.lane ^ 32) << 2, __builtin_bit_cast(int, send))); }
; #pragma unroll
;               for (int m = 0; m < 4; ++m) { const float keep = hi4 ? r8[4 + m] : r8[m], send = hi4 ? r8[m] : r8[4 + m];
;                   r4[m] = keep + __builtin_bit_cast(float, __builtin_amdgcn_ds_bpermute((F.lane ^ 16) << 2, __builtin_bit_cast(int, send))); }
;               int lo3_ = lo_; asm volatile("" : "+v"(lo3_));
;               const size_t col = (size_t)t * D_ + (size_t)(unsigned)(256 * c + lo3_);
;               const f32x4 o = {r4[0] + bflo(hb.x), r4[1] + bfhi(hb.x), r4[2] + bflo(hb.y), r4[3] + bfhi(hb.y)};
;               SSQ[i * 64 + F.lane] += (o.x * o.x + o.y * o.y) + (o.z * o.z + o.w * o.w);
;               *(f32x4*)(F.out + col) = o;
;     ...
;       __builtin_amdgcn_fence(__ATOMIC_SEQ_CST, "agent");
;       const int l2_ = fresh_lane(), lo2_ = 16 * (l2_ & 15) + 4 * (l2_ >> 4);
; #pragma unroll
;       for (int i = 0; i < 4; ++i) { const int t = F.gw + i * F.NGW;
;           const float rs = 1.0f / sqrtf(wave_sum(SSQ[i * 64 + l2_]) * (1.f / D_) + 1e-6f);
; _Pragma("nounroll")
;           for (int c0 = 0; c0 < 16; c0 += 8) {
; #pragma unroll
;               for (int c = c0; c < c0 + 8; ++c) { const size_t col = (size_t)t * D_ + (size_t)(unsigned)(256 * c + lo2_); const f32x4 gn = *(const f32x4*)(lnf + (256 * c + lo2_));
;                   const f32x4 o = *(const f32x4*)(F.out + col);
	v_mov_b32_e32 v184, v221
	v_pk_fma_f32 v[0:1], v[0:1], v[220:221], v[32:33] op_sel_hi:[1,0,1]
	v_pk_fma_f32 v[2:3], v[2:3], v[220:221], v[34:35] op_sel_hi:[1,0,1]
	v_pk_fma_f32 v[4:5], v[4:5], v[220:221], v[36:37] op_sel_hi:[1,0,1]
	v_pk_fma_f32 v[6:7], v[6:7], v[220:221], v[38:39] op_sel_hi:[1,0,1]
	v_pk_fma_f32 v[8:9], v[8:9], v[220:221], v[40:41] op_sel_hi:[1,0,1]
	v_pk_fma_f32 v[10:11], v[10:11], v[220:221], v[42:43] op_sel_hi:[1,0,1]
	v_pk_fma_f32 v[12:13], v[12:13], v[220:221], v[44:45] op_sel_hi:[1,0,1]
	v_pk_fma_f32 v[14:15], v[14:15], v[220:221], v[46:47] op_sel_hi:[1,0,1]
	v_pk_fma_f32 v[0:1], v[16:17], v[184:185], v[0:1] op_sel_hi:[1,0,1]
	v_pk_fma_f32 v[2:3], v[18:19], v[184:185], v[2:3] op_sel_hi:[1,0,1]
	v_pk_fma_f32 v[4:5], v[20:21], v[184:185], v[4:5] op_sel_hi:[1,0,1]
	v_pk_fma_f32 v[6:7], v[22:23], v[184:185], v[6:7] op_sel_hi:[1,0,1]
	v_pk_fma_f32 v[8:9], v[24:25], v[184:185], v[8:9] op_sel_hi:[1,0,1]
	v_pk_fma_f32 v[10:11], v[26:27], v[184:185], v[10:11] op_sel_hi:[1,0,1]
	v_pk_fma_f32 v[12:13], v[28:29], v[184:185], v[12:13] op_sel_hi:[1,0,1]
	v_pk_fma_f32 v[14:15], v[30:31], v[184:185], v[14:15] op_sel_hi:[1,0,1]
	v_cndmask_b32_e32 v18, v0, v8, vcc
	v_cndmask_b32_e32 v19, v1, v9, vcc
	v_cndmask_b32_e32 v20, v2, v10, vcc
	v_cndmask_b32_e32 v21, v3, v11, vcc
	v_cndmask_b32_e32 v22, v4, v12, vcc
	v_cndmask_b32_e32 v23, v5, v13, vcc
	v_cndmask_b32_e32 v24, v6, v14, vcc
	v_cndmask_b32_e32 v25, v7, v15, vcc
	v_cndmask_b32_e32 v17, v10, v2, vcc
	v_cndmask_b32_e32 v16, v8, v0, vcc
	v_cndmask_b32_e32 v3, v11, v3, vcc
	v_cndmask_b32_e32 v2, v9, v1, vcc
	v_cndmask_b32_e32 v1, v14, v6, vcc
	v_cndmask_b32_e32 v0, v12, v4, vcc
	v_cndmask_b32_e32 v6, v13, v5, vcc
	ds_bpermute_b32 v4, v171, v18
	ds_bpermute_b32 v8, v171, v19
	ds_bpermute_b32 v5, v171, v20
	ds_bpermute_b32 v9, v171, v21
	ds_bpermute_b32 v10, v171, v22
	ds_bpermute_b32 v12, v171, v23
	ds_bpermute_b32 v11, v171, v24
	ds_bpermute_b32 v13, v171, v25
	v_cndmask_b32_e32 v7, v15, v7, vcc
	s_waitcnt lgkmcnt(5)
	v_pk_add_f32 v[4:5], v[16:17], v[4:5]
	s_waitcnt lgkmcnt(4)
	v_pk_add_f32 v[2:3], v[2:3], v[8:9]
	s_waitcnt lgkmcnt(1)
	v_pk_add_f32 v[0:1], v[0:1], v[10:11]
	s_waitcnt lgkmcnt(0)
	v_pk_add_f32 v[6:7], v[6:7], v[12:13]
	v_cndmask_b32_e64 v10, v4, v0, s[0:1]
	v_cndmask_b32_e64 v11, v2, v6, s[0:1]
	v_cndmask_b32_e64 v9, v1, v5, s[0:1]
	v_cndmask_b32_e64 v8, v0, v4, s[0:1]
	v_cndmask_b32_e64 v5, v5, v1, s[0:1]
	v_cndmask_b32_e64 v0, v6, v2, s[0:1]
	v_cndmask_b32_e64 v6, v3, v7, s[0:1]
	v_cndmask_b32_e64 v1, v7, v3, s[0:1]
	ds_bpermute_b32 v2, v170, v10
	ds_bpermute_b32 v4, v170, v11
	ds_bpermute_b32 v3, v170, v5
	ds_bpermute_b32 v5, v170, v6
	v_add_u32_e32 v178, s28, v174
	ds_read_b32 v155, v178
	s_addk_i32 s28, 0x100
	s_waitcnt lgkmcnt(2)
	v_pk_add_f32 v[2:3], v[8:9], v[2:3]
	s_waitcnt lgkmcnt(1)
	v_pk_add_f32 v[0:1], v[0:1], v[4:5]
	v_pk_add_f32 v[4:5], v[2:3], v[166:167]
	v_pk_add_f32 v[2:3], v[0:1], v[168:169]
	v_mov_b32_e32 v0, v4
	v_pk_mul_f32 v[6:7], v[2:3], v[2:3]
	v_mov_b32_e32 v1, v2
	v_mov_b32_e32 v2, v5
	v_pk_fma_f32 v[4:5], v[4:5], v[4:5], v[6:7]
	s_addk_i32 s23, 0x80
	s_add_i32 s12, s12, s34
	global_store_dwordx4 v[180:181], v[0:3], off
	s_cmpk_eq_i32 s28, 0x400
	v_add_u32_e32 v177, 0x200, v177
	v_add_f32_e32 v0, v4, v5
	s_waitcnt vmcnt(1)
	v_mov_b32_e32 v149, v202
	v_mov_b32_e32 v150, v203
	v_mov_b32_e32 v151, v204
	v_mov_b32_e32 v143, v198
	v_mov_b32_e32 v144, v199
	v_mov_b32_e32 v145, v200
	v_mov_b32_e32 v131, v156
	v_mov_b32_e32 v132, v157
	v_mov_b32_e32 v133, v158
	v_mov_b32_e32 v137, v152
	v_mov_b32_e32 v138, v153
	v_mov_b32_e32 v139, v154
	s_waitcnt lgkmcnt(0)
	v_add_f32_e32 v0, v155, v0
	ds_write_b32 v178, v0
	s_cbranch_scc0 .LBB0_3403
	s_cmp_eq_u32 s19, 16
	s_mov_b32 s17, s19
	s_cbranch_scc0 .LBB0_3402
	s_waitcnt vmcnt(0) lgkmcnt(0)
	buffer_inv sc1
	v_mbcnt_lo_u32_b32 v0, -1, 0
	v_mbcnt_hi_u32_b32 v0, -1, v0
	v_lshl_add_u32 v7, v0, 2, s20
	v_and_b32_e32 v2, 15, v0
	v_lshrrev_b32_e32 v3, 4, v0
	v_lshlrev_b32_e32 v2, 6, v2
	v_lshl_add_u32 v6, v3, 4, v2
	v_add_u32_e32 v10, 0x1000, v6
	v_add_u32_e32 v11, 0x2000, v6
	v_add_u32_e32 v12, 0x3000, v6
	s_lshl_b64 s[0:1], s[94:95], 14
	s_add_u32 s12, s26, s0
	s_addc_u32 s13, s27, s1
	s_lshl_b64 s[0:1], s[4:5], 14
	s_add_u32 s14, s26, s0
	s_addc_u32 s15, s27, s1
	s_lshl_b64 s[0:1], s[8:9], 14
	s_add_u32 s16, s26, s0
	s_addc_u32 s17, s27, s1
	s_lshl_b64 s[0:1], s[10:11], 14
	s_add_u32 s18, s26, s0
	s_addc_u32 s19, s27, s1
	global_load_dwordx4 v[60:63], v6, s[24:25] offset:0
	global_load_dwordx4 v[64:67], v6, s[24:25] offset:1024
	global_load_dwordx4 v[68:71], v6, s[24:25] offset:2048
	global_load_dwordx4 v[72:75], v6, s[24:25] offset:3072
	global_load_dwordx4 v[76:79], v10, s[24:25] offset:0
	global_load_dwordx4 v[80:83], v10, s[24:25] offset:1024
	global_load_dwordx4 v[84:87], v10, s[24:25] offset:2048
	global_load_dwordx4 v[88:91], v10, s[24:25] offset:3072
	global_load_dwordx4 v[92:95], v11, s[24:25] offset:0
	global_load_dwordx4 v[96:99], v11, s[24:25] offset:1024
	global_load_dwordx4 v[100:103], v11, s[24:25] offset:2048
	global_load_dwordx4 v[104:107], v11, s[24:25] offset:3072
	global_load_dwordx4 v[108:111], v12, s[24:25] offset:0
	global_load_dwordx4 v[112:115], v12, s[24:25] offset:1024
	global_load_dwordx4 v[116:119], v12, s[24:25] offset:2048
	global_load_dwordx4 v[120:123], v12, s[24:25] offset:3072
	global_load_dwordx4 v[124:127], v6, s[12:13] offset:0
	global_load_dwordx4 v[128:131], v6, s[12:13] offset:1024
	global_load_dwordx4 v[132:135], v6, s[12:13] offset:2048
	global_load_dwordx4 v[136:139], v6, s[12:13] offset:3072
	global_load_dwordx4 v[140:143], v10, s[12:13] offset:0
; __device__ __forceinline__ int fresh_lane() { int l; asm volatile("v_mbcnt_lo_u32_b32 %0, -1, 0\n\tv_mbcnt_hi_u32_b32 %0, -1, %0" : "=v"(l)); return l; }
; __device__ __forceinline__ float wave_sum(float v) { v = dpp_add16(v); return (rdlane(v, 0) + rdlane(v, 16)) + (rdlane(v, 32) + rdlane(v, 48)); }
; __device__ __forceinline__ void p12_peer(Frame& F) {
;     ...
;       const int l2_ = fresh_lane(), lo2_ = 16 * (l2_ & 15) + 4 * (l2_ >> 4);
; #pragma unroll
;       for (int i = 0; i < 4; ++i) { const int t = F.gw + i * F.NGW;
;           const float rs = 1.0f / sqrtf(wave_sum(SSQ[i * 64 + l2_]) * (1.f / D_) + 1e-6f);
; _Pragma("nounroll")
;           for (int c0 = 0; c0 < 16; c0 += 8) {
; #pragma unroll
;               for (int c = c0; c < c0 + 8; ++c) { const size_t col = (size_t)t * D_ + (size_t)(unsigned)(256 * c + lo2_); const f32x4 gn = *(const f32x4*)(lnf + (256 * c + lo2_));
	global_load_dwordx4 v[144:147], v10, s[12:13] offset:1024
	global_load_dwordx4 v[148:151], v10, s[12:13] offset:2048
	global_load_dwordx4 v[152:155], v10, s[12:13] offset:3072
	global_load_dwordx4 v[156:159], v11, s[12:13] offset:0
	global_load_dwordx4 v[160:163], v11, s[12:13] offset:1024
	global_load_dwordx4 v[164:167], v11, s[12:13] offset:2048
	global_load_dwordx4 v[168:171], v11, s[12:13] offset:3072
	global_load_dwordx4 v[172:175], v12, s[12:13] offset:0
	global_load_dwordx4 v[176:179], v12, s[12:13] offset:1024
	global_load_dwordx4 v[180:183], v12, s[12:13] offset:2048
	global_load_dwordx4 v[184:187], v12, s[12:13] offset:3072
	global_load_dwordx4 v[188:191], v6, s[14:15] offset:0
	global_load_dwordx4 v[192:195], v6, s[14:15] offset:1024
	global_load_dwordx4 v[196:199], v6, s[14:15] offset:2048
	global_load_dwordx4 v[200:203], v6, s[14:15] offset:3072
	global_load_dwordx4 v[204:207], v10, s[14:15] offset:0
	global_load_dwordx4 v[208:211], v10, s[14:15] offset:1024
	global_load_dwordx4 v[212:215], v10, s[14:15] offset:2048
	global_load_dwordx4 v[216:219], v10, s[14:15] offset:3072
	global_load_dwordx4 v[220:223], v11, s[14:15] offset:0
	global_load_dwordx4 v[224:227], v11, s[14:15] offset:1024
	global_load_dwordx4 v[228:231], v11, s[14:15] offset:2048
	global_load_dwordx4 v[232:235], v11, s[14:15] offset:3072
	global_load_dwordx4 v[236:239], v12, s[14:15] offset:0
	global_load_dwordx4 v[240:243], v12, s[14:15] offset:1024
	global_load_dwordx4 v[244:247], v12, s[14:15] offset:2048
	global_load_dwordx4 v[248:251], v12, s[14:15] offset:3072
	ds_read_b32 v1, v7 offset:4096
	s_waitcnt lgkmcnt(0)
	v_add_f32_dpp v1, v1, v1 quad_perm:[1,0,3,2] row_mask:0xf bank_mask:0xf bound_ctrl:1
	s_nop 1
	v_add_f32_dpp v1, v1, v1 quad_perm:[2,3,0,1] row_mask:0xf bank_mask:0xf bound_ctrl:1
	s_nop 1
	v_add_f32_dpp v1, v1, v1 row_half_mirror row_mask:0xf bank_mask:0xf bound_ctrl:1
	s_nop 1
	v_add_f32_dpp v1, v1, v1 row_mirror row_mask:0xf bank_mask:0xf bound_ctrl:1
	s_nop 0
	v_readlane_b32 s1, v1, 16
	v_readlane_b32 s0, v1, 0
	s_nop 0
	v_mov_b32_e32 v3, s1
	v_readlane_b32 s1, v1, 48
	v_add_f32_e32 v3, s0, v3
	v_readlane_b32 s0, v1, 32
	v_mov_b32_e32 v1, s1
	s_nop 0
	v_add_f32_e32 v1, s0, v1
	v_add_f32_e32 v1, v3, v1
	v_mov_b32_e32 v3, 0x358637bd
	v_fmac_f32_e32 v3, 0x39800000, v1
	s_mov_b32 s0, 0xf800000
	v_mul_f32_e32 v1, 0x4f800000, v3
	v_cmp_gt_f32_e32 vcc, s0, v3
	s_nop 1
	v_cndmask_b32_e32 v1, v3, v1, vcc
	v_sqrt_f32_e32 v3, v1
	s_nop 0
	v_add_u32_e32 v4, -1, v3
	v_fma_f32 v5, -v4, v3, v1
	v_cmp_ge_f32_e64 s[0:1], 0, v5
	v_add_u32_e32 v5, 1, v3
	s_nop 0
	v_cndmask_b32_e64 v4, v3, v4, s[0:1]
	v_fma_f32 v3, -v5, v3, v1
	v_cmp_lt_f32_e64 s[0:1], 0, v3
	s_nop 1
	v_cndmask_b32_e64 v3, v4, v5, s[0:1]
	v_mul_f32_e32 v4, 0x37800000, v3
	v_cndmask_b32_e32 v3, v3, v4, vcc
	v_mov_b32_e32 v4, 0x260
	v_cmp_class_f32_e32 vcc, v1, v4
	s_nop 1
	v_cndmask_b32_e32 v3, v3, v1, vcc
	v_div_scale_f32 v4, s[0:1], v3, v3, 1.0
	v_rcp_f32_e32 v5, v4
	s_nop 0
	v_fma_f32 v0, -v4, v5, 1.0
	v_fmac_f32_e32 v5, v0, v5
	v_div_scale_f32 v0, vcc, 1.0, v3, 1.0
	v_mul_f32_e32 v2, v0, v5
	v_fma_f32 v8, -v4, v2, v0
	v_fmac_f32_e32 v2, v8, v5
	v_fma_f32 v0, -v4, v2, v0
	v_div_fmas_f32 v0, v0, v5, v2
	v_div_fixup_f32 v2, v0, v3, 1.0
	v_mov_b32_e32 v40, v2
	v_mov_b32_e32 v41, v2
	ds_read_b32 v1, v7 offset:4352
	s_waitcnt lgkmcnt(0)
	v_add_f32_dpp v1, v1, v1 quad_perm:[1,0,3,2] row_mask:0xf bank_mask:0xf bound_ctrl:1
	s_nop 1
	v_add_f32_dpp v1, v1, v1 quad_perm:[2,3,0,1] row_mask:0xf bank_mask:0xf bound_ctrl:1
	s_nop 1
	v_add_f32_dpp v1, v1, v1 row_half_mirror row_mask:0xf bank_mask:0xf bound_ctrl:1
	s_nop 1
	v_add_f32_dpp v1, v1, v1 row_mirror row_mask:0xf bank_mask:0xf bound_ctrl:1
	s_nop 0
	v_readlane_b32 s1, v1, 16
	v_readlane_b32 s0, v1, 0
	s_nop 0
	v_mov_b32_e32 v3, s1
	v_readlane_b32 s1, v1, 48
	v_add_f32_e32 v3, s0, v3
	v_readlane_b32 s0, v1, 32
	v_mov_b32_e32 v1, s1
	s_nop 0
	v_add_f32_e32 v1, s0, v1
	v_add_f32_e32 v1, v3, v1
	v_mov_b32_e32 v3, 0x358637bd
	v_fmac_f32_e32 v3, 0x39800000, v1
	s_mov_b32 s0, 0xf800000
	v_mul_f32_e32 v1, 0x4f800000, v3
	v_cmp_gt_f32_e32 vcc, s0, v3
	s_nop 1
	v_cndmask_b32_e32 v1, v3, v1, vcc
	v_sqrt_f32_e32 v3, v1
	s_nop 0
	v_add_u32_e32 v4, -1, v3
	v_fma_f32 v5, -v4, v3, v1
	v_cmp_ge_f32_e64 s[0:1], 0, v5
	v_add_u32_e32 v5, 1, v3
	s_nop 0
	v_cndmask_b32_e64 v4, v3, v4, s[0:1]
	v_fma_f32 v3, -v5, v3, v1
	v_cmp_lt_f32_e64 s[0:1], 0, v3
	s_nop 1
	v_cndmask_b32_e64 v3, v4, v5, s[0:1]
	v_mul_f32_e32 v4, 0x37800000, v3
	v_cndmask_b32_e32 v3, v3, v4, vcc
	v_mov_b32_e32 v4, 0x260
	v_cmp_class_f32_e32 vcc, v1, v4
	s_nop 1
	v_cndmask_b32_e32 v3, v3, v1, vcc
	v_div_scale_f32 v4, s[0:1], v3, v3, 1.0
	v_rcp_f32_e32 v5, v4
	s_nop 0
	v_fma_f32 v0, -v4, v5, 1.0
	v_fmac_f32_e32 v5, v0, v5
	v_div_scale_f32 v0, vcc, 1.0, v3, 1.0
	v_mul_f32_e32 v2, v0, v5
	v_fma_f32 v8, -v4, v2, v0
	v_fmac_f32_e32 v2, v8, v5
	v_fma_f32 v0, -v4, v2, v0
	v_div_fmas_f32 v0, v0, v5, v2
	v_div_fixup_f32 v2, v0, v3, 1.0
	v_mov_b32_e32 v42, v2
	v_mov_b32_e32 v43, v2
	ds_read_b32 v1, v7 offset:4608
	s_waitcnt lgkmcnt(0)
; __device__ __forceinline__ float wave_sum(float v) { v = dpp_add16(v); return (rdlane(v, 0) + rdlane(v, 16)) + (rdlane(v, 32) + rdlane(v, 48)); }
; __device__ __forceinline__ void p12_peer(Frame& F) {
;     ...
;       for (int i = 0; i < 4; ++i) { const int t = F.gw + i * F.NGW;
;           const float rs = 1.0f / sqrtf(wave_sum(SSQ[i * 64 + l2_]) * (1.f / D_) + 1e-6f);
; _Pragma("nounroll")
;           for (int c0 = 0; c0 < 16; c0 += 8) {
; #pragma unroll
;               for (int c = c0; c < c0 + 8; ++c) { const size_t col = (size_t)t * D_ + (size_t)(unsigned)(256 * c + lo2_); const f32x4 gn = *(const f32x4*)(lnf + (256 * c + lo2_));
;                   const f32x4 o = *(const f32x4*)(F.out + col);
;                   *(f32x4*)(F.out + col) = (f32x4){o.x * rs * gn.x, o.y * rs * gn.y, o.z * rs * gn.z, o.w * rs * gn.w}; }
	v_add_f32_dpp v1, v1, v1 quad_perm:[1,0,3,2] row_mask:0xf bank_mask:0xf bound_ctrl:1
	s_nop 1
	v_add_f32_dpp v1, v1, v1 quad_perm:[2,3,0,1] row_mask:0xf bank_mask:0xf bound_ctrl:1
	s_nop 1
	v_add_f32_dpp v1, v1, v1 row_half_mirror row_mask:0xf bank_mask:0xf bound_ctrl:1
	s_nop 1
	v_add_f32_dpp v1, v1, v1 row_mirror row_mask:0xf bank_mask:0xf bound_ctrl:1
	s_nop 0
	v_readlane_b32 s1, v1, 16
	v_readlane_b32 s0, v1, 0
	s_nop 0
	v_mov_b32_e32 v3, s1
	v_readlane_b32 s1, v1, 48
	v_add_f32_e32 v3, s0, v3
	v_readlane_b32 s0, v1, 32
	v_mov_b32_e32 v1, s1
	s_nop 0
	v_add_f32_e32 v1, s0, v1
	v_add_f32_e32 v1, v3, v1
	v_mov_b32_e32 v3, 0x358637bd
	v_fmac_f32_e32 v3, 0x39800000, v1
	s_mov_b32 s0, 0xf800000
	v_mul_f32_e32 v1, 0x4f800000, v3
	v_cmp_gt_f32_e32 vcc, s0, v3
	s_nop 1
	v_cndmask_b32_e32 v1, v3, v1, vcc
	v_sqrt_f32_e32 v3, v1
	s_nop 0
	v_add_u32_e32 v4, -1, v3
	v_fma_f32 v5, -v4, v3, v1
	v_cmp_ge_f32_e64 s[0:1], 0, v5
	v_add_u32_e32 v5, 1, v3
	s_nop 0
	v_cndmask_b32_e64 v4, v3, v4, s[0:1]
	v_fma_f32 v3, -v5, v3, v1
	v_cmp_lt_f32_e64 s[0:1], 0, v3
	s_nop 1
	v_cndmask_b32_e64 v3, v4, v5, s[0:1]
	v_mul_f32_e32 v4, 0x37800000, v3
	v_cndmask_b32_e32 v3, v3, v4, vcc
	v_mov_b32_e32 v4, 0x260
	v_cmp_class_f32_e32 vcc, v1, v4
	s_nop 1
	v_cndmask_b32_e32 v3, v3, v1, vcc
	v_div_scale_f32 v4, s[0:1], v3, v3, 1.0
	v_rcp_f32_e32 v5, v4
	s_nop 0
	v_fma_f32 v0, -v4, v5, 1.0
	v_fmac_f32_e32 v5, v0, v5
	v_div_scale_f32 v0, vcc, 1.0, v3, 1.0
	v_mul_f32_e32 v2, v0, v5
	v_fma_f32 v8, -v4, v2, v0
	v_fmac_f32_e32 v2, v8, v5
	v_fma_f32 v0, -v4, v2, v0
	v_div_fmas_f32 v0, v0, v5, v2
	v_div_fixup_f32 v2, v0, v3, 1.0
	v_mov_b32_e32 v44, v2
	v_mov_b32_e32 v45, v2
	ds_read_b32 v1, v7 offset:4864
	s_waitcnt lgkmcnt(0)
	v_add_f32_dpp v1, v1, v1 quad_perm:[1,0,3,2] row_mask:0xf bank_mask:0xf bound_ctrl:1
	s_nop 1
	v_add_f32_dpp v1, v1, v1 quad_perm:[2,3,0,1] row_mask:0xf bank_mask:0xf bound_ctrl:1
	s_nop 1
	v_add_f32_dpp v1, v1, v1 row_half_mirror row_mask:0xf bank_mask:0xf bound_ctrl:1
	s_nop 1
	v_add_f32_dpp v1, v1, v1 row_mirror row_mask:0xf bank_mask:0xf bound_ctrl:1
	s_nop 0
	v_readlane_b32 s1, v1, 16
	v_readlane_b32 s0, v1, 0
	s_nop 0
	v_mov_b32_e32 v3, s1
	v_readlane_b32 s1, v1, 48
	v_add_f32_e32 v3, s0, v3
	v_readlane_b32 s0, v1, 32
	v_mov_b32_e32 v1, s1
	s_nop 0
	v_add_f32_e32 v1, s0, v1
	v_add_f32_e32 v1, v3, v1
	v_mov_b32_e32 v3, 0x358637bd
	v_fmac_f32_e32 v3, 0x39800000, v1
	s_mov_b32 s0, 0xf800000
	v_mul_f32_e32 v1, 0x4f800000, v3
	v_cmp_gt_f32_e32 vcc, s0, v3
	s_nop 1
	v_cndmask_b32_e32 v1, v3, v1, vcc
	v_sqrt_f32_e32 v3, v1
	s_nop 0
	v_add_u32_e32 v4, -1, v3
	v_fma_f32 v5, -v4, v3, v1
	v_cmp_ge_f32_e64 s[0:1], 0, v5
	v_add_u32_e32 v5, 1, v3
	s_nop 0
	v_cndmask_b32_e64 v4, v3, v4, s[0:1]
	v_fma_f32 v3, -v5, v3, v1
	v_cmp_lt_f32_e64 s[0:1], 0, v3
	s_nop 1
	v_cndmask_b32_e64 v3, v4, v5, s[0:1]
	v_mul_f32_e32 v4, 0x37800000, v3
	v_cndmask_b32_e32 v3, v3, v4, vcc
	v_mov_b32_e32 v4, 0x260
	v_cmp_class_f32_e32 vcc, v1, v4
	s_nop 1
	v_cndmask_b32_e32 v3, v3, v1, vcc
	v_div_scale_f32 v4, s[0:1], v3, v3, 1.0
	v_rcp_f32_e32 v5, v4
	s_nop 0
	v_fma_f32 v0, -v4, v5, 1.0
	v_fmac_f32_e32 v5, v0, v5
	v_div_scale_f32 v0, vcc, 1.0, v3, 1.0
	v_mul_f32_e32 v2, v0, v5
	v_fma_f32 v8, -v4, v2, v0
	v_fmac_f32_e32 v2, v8, v5
	v_fma_f32 v0, -v4, v2, v0
	v_div_fmas_f32 v0, v0, v5, v2
	v_div_fixup_f32 v2, v0, v3, 1.0
	v_mov_b32_e32 v46, v2
	v_mov_b32_e32 v47, v2
	s_waitcnt vmcnt(31)
	v_pk_mul_f32 v[124:125], v[40:41], v[124:125]
	v_pk_mul_f32 v[126:127], v[40:41], v[126:127]
	v_pk_mul_f32 v[124:125], v[60:61], v[124:125]
	v_pk_mul_f32 v[126:127], v[62:63], v[126:127]
	global_store_dwordx4 v6, v[124:127], s[12:13] offset:0 nt
	s_waitcnt vmcnt(31)
	v_pk_mul_f32 v[128:129], v[40:41], v[128:129]
	v_pk_mul_f32 v[130:131], v[40:41], v[130:131]
	v_pk_mul_f32 v[128:129], v[64:65], v[128:129]
	v_pk_mul_f32 v[130:131], v[66:67], v[130:131]
	global_store_dwordx4 v6, v[128:131], s[12:13] offset:1024 nt
	s_waitcnt vmcnt(31)
	v_pk_mul_f32 v[132:133], v[40:41], v[132:133]
	v_pk_mul_f32 v[134:135], v[40:41], v[134:135]
	v_pk_mul_f32 v[132:133], v[68:69], v[132:133]
	v_pk_mul_f32 v[134:135], v[70:71], v[134:135]
	global_store_dwordx4 v6, v[132:135], s[12:13] offset:2048 nt
	s_waitcnt vmcnt(31)
	v_pk_mul_f32 v[136:137], v[40:41], v[136:137]
	v_pk_mul_f32 v[138:139], v[40:41], v[138:139]
	v_pk_mul_f32 v[136:137], v[72:73], v[136:137]
	v_pk_mul_f32 v[138:139], v[74:75], v[138:139]
	global_store_dwordx4 v6, v[136:139], s[12:13] offset:3072 nt
	s_waitcnt vmcnt(31)
	v_pk_mul_f32 v[140:141], v[40:41], v[140:141]
	v_pk_mul_f32 v[142:143], v[40:41], v[142:143]
	v_pk_mul_f32 v[140:141], v[76:77], v[140:141]
	v_pk_mul_f32 v[142:143], v[78:79], v[142:143]
	global_store_dwordx4 v10, v[140:143], s[12:13] offset:0 nt
	s_waitcnt vmcnt(31)
	v_pk_mul_f32 v[144:145], v[40:41], v[144:145]
	v_pk_mul_f32 v[146:147], v[40:41], v[146:147]
	v_pk_mul_f32 v[144:145], v[80:81], v[144:145]
	v_pk_mul_f32 v[146:147], v[82:83], v[146:147]
	global_store_dwordx4 v10, v[144:147], s[12:13] offset:1024 nt
	s_waitcnt vmcnt(31)
	v_pk_mul_f32 v[148:149], v[40:41], v[148:149]
	v_pk_mul_f32 v[150:151], v[40:41], v[150:151]
	v_pk_mul_f32 v[148:149], v[84:85], v[148:149]
	v_pk_mul_f32 v[150:151], v[86:87], v[150:151]
	global_store_dwordx4 v10, v[148:151], s[12:13] offset:2048 nt
	s_waitcnt vmcnt(31)
	v_pk_mul_f32 v[152:153], v[40:41], v[152:153]
	v_pk_mul_f32 v[154:155], v[40:41], v[154:155]
	v_pk_mul_f32 v[152:153], v[88:89], v[152:153]
	v_pk_mul_f32 v[154:155], v[90:91], v[154:155]
	global_store_dwordx4 v10, v[152:155], s[12:13] offset:3072 nt
	s_waitcnt vmcnt(31)
; __device__ __forceinline__ void p12_peer(Frame& F) {
;     ...
;           for (int c0 = 0; c0 < 16; c0 += 8) {
; #pragma unroll
;               for (int c = c0; c < c0 + 8; ++c) { const size_t col = (size_t)t * D_ + (size_t)(unsigned)(256 * c + lo2_); const f32x4 gn = *(const f32x4*)(lnf + (256 * c + lo2_));
;                   const f32x4 o = *(const f32x4*)(F.out + col);
;                   *(f32x4*)(F.out + col) = (f32x4){o.x * rs * gn.x, o.y * rs * gn.y, o.z * rs * gn.z, o.w * rs * gn.w}; }
;               asm volatile("" ::: "memory"); } }
	v_pk_mul_f32 v[156:157], v[40:41], v[156:157]
	v_pk_mul_f32 v[158:159], v[40:41], v[158:159]
	v_pk_mul_f32 v[156:157], v[92:93], v[156:157]
	v_pk_mul_f32 v[158:159], v[94:95], v[158:159]
	global_store_dwordx4 v11, v[156:159], s[12:13] offset:0 nt
	s_waitcnt vmcnt(31)
	v_pk_mul_f32 v[160:161], v[40:41], v[160:161]
	v_pk_mul_f32 v[162:163], v[40:41], v[162:163]
	v_pk_mul_f32 v[160:161], v[96:97], v[160:161]
	v_pk_mul_f32 v[162:163], v[98:99], v[162:163]
	global_store_dwordx4 v11, v[160:163], s[12:13] offset:1024 nt
	s_waitcnt vmcnt(31)
	v_pk_mul_f32 v[164:165], v[40:41], v[164:165]
	v_pk_mul_f32 v[166:167], v[40:41], v[166:167]
	v_pk_mul_f32 v[164:165], v[100:101], v[164:165]
	v_pk_mul_f32 v[166:167], v[102:103], v[166:167]
	global_store_dwordx4 v11, v[164:167], s[12:13] offset:2048 nt
	s_waitcnt vmcnt(31)
	v_pk_mul_f32 v[168:169], v[40:41], v[168:169]
	v_pk_mul_f32 v[170:171], v[40:41], v[170:171]
	v_pk_mul_f32 v[168:169], v[104:105], v[168:169]
	v_pk_mul_f32 v[170:171], v[106:107], v[170:171]
	global_store_dwordx4 v11, v[168:171], s[12:13] offset:3072 nt
	s_waitcnt vmcnt(31)
	v_pk_mul_f32 v[172:173], v[40:41], v[172:173]
	v_pk_mul_f32 v[174:175], v[40:41], v[174:175]
	v_pk_mul_f32 v[172:173], v[108:109], v[172:173]
	v_pk_mul_f32 v[174:175], v[110:111], v[174:175]
	global_store_dwordx4 v12, v[172:175], s[12:13] offset:0 nt
	s_waitcnt vmcnt(31)
	v_pk_mul_f32 v[176:177], v[40:41], v[176:177]
	v_pk_mul_f32 v[178:179], v[40:41], v[178:179]
	v_pk_mul_f32 v[176:177], v[112:113], v[176:177]
	v_pk_mul_f32 v[178:179], v[114:115], v[178:179]
	global_store_dwordx4 v12, v[176:179], s[12:13] offset:1024 nt
	s_waitcnt vmcnt(31)
	v_pk_mul_f32 v[180:181], v[40:41], v[180:181]
	v_pk_mul_f32 v[182:183], v[40:41], v[182:183]
	v_pk_mul_f32 v[180:181], v[116:117], v[180:181]
	v_pk_mul_f32 v[182:183], v[118:119], v[182:183]
	global_store_dwordx4 v12, v[180:183], s[12:13] offset:2048 nt
	s_waitcnt vmcnt(31)
	v_pk_mul_f32 v[184:185], v[40:41], v[184:185]
	v_pk_mul_f32 v[186:187], v[40:41], v[186:187]
	v_pk_mul_f32 v[184:185], v[120:121], v[184:185]
	v_pk_mul_f32 v[186:187], v[122:123], v[186:187]
	global_store_dwordx4 v12, v[184:187], s[12:13] offset:3072 nt
	s_nop 1
	global_load_dwordx4 v[124:127], v6, s[16:17] offset:0
	global_load_dwordx4 v[128:131], v6, s[16:17] offset:1024
	global_load_dwordx4 v[132:135], v6, s[16:17] offset:2048
	global_load_dwordx4 v[136:139], v6, s[16:17] offset:3072
	global_load_dwordx4 v[140:143], v10, s[16:17] offset:0
	global_load_dwordx4 v[144:147], v10, s[16:17] offset:1024
	global_load_dwordx4 v[148:151], v10, s[16:17] offset:2048
	global_load_dwordx4 v[152:155], v10, s[16:17] offset:3072
	global_load_dwordx4 v[156:159], v11, s[16:17] offset:0
	global_load_dwordx4 v[160:163], v11, s[16:17] offset:1024
	global_load_dwordx4 v[164:167], v11, s[16:17] offset:2048
	global_load_dwordx4 v[168:171], v11, s[16:17] offset:3072
	global_load_dwordx4 v[172:175], v12, s[16:17] offset:0
	global_load_dwordx4 v[176:179], v12, s[16:17] offset:1024
	global_load_dwordx4 v[180:183], v12, s[16:17] offset:2048
	global_load_dwordx4 v[184:187], v12, s[16:17] offset:3072
	s_waitcnt vmcnt(47)
	v_pk_mul_f32 v[188:189], v[42:43], v[188:189]
	v_pk_mul_f32 v[190:191], v[42:43], v[190:191]
	v_pk_mul_f32 v[188:189], v[60:61], v[188:189]
	v_pk_mul_f32 v[190:191], v[62:63], v[190:191]
	global_store_dwordx4 v6, v[188:191], s[14:15] offset:0 nt
	s_waitcnt vmcnt(47)
	v_pk_mul_f32 v[192:193], v[42:43], v[192:193]
	v_pk_mul_f32 v[194:195], v[42:43], v[194:195]
	v_pk_mul_f32 v[192:193], v[64:65], v[192:193]
	v_pk_mul_f32 v[194:195], v[66:67], v[194:195]
	global_store_dwordx4 v6, v[192:195], s[14:15] offset:1024 nt
	s_waitcnt vmcnt(47)
	v_pk_mul_f32 v[196:197], v[42:43], v[196:197]
	v_pk_mul_f32 v[198:199], v[42:43], v[198:199]
	v_pk_mul_f32 v[196:197], v[68:69], v[196:197]
	v_pk_mul_f32 v[198:199], v[70:71], v[198:199]
	global_store_dwordx4 v6, v[196:199], s[14:15] offset:2048 nt
	s_waitcnt vmcnt(47)
	v_pk_mul_f32 v[200:201], v[42:43], v[200:201]
	v_pk_mul_f32 v[202:203], v[42:43], v[202:203]
	v_pk_mul_f32 v[200:201], v[72:73], v[200:201]
	v_pk_mul_f32 v[202:203], v[74:75], v[202:203]
	global_store_dwordx4 v6, v[200:203], s[14:15] offset:3072 nt
	s_waitcnt vmcnt(47)
	v_pk_mul_f32 v[204:205], v[42:43], v[204:205]
	v_pk_mul_f32 v[206:207], v[42:43], v[206:207]
	v_pk_mul_f32 v[204:205], v[76:77], v[204:205]
	v_pk_mul_f32 v[206:207], v[78:79], v[206:207]
	global_store_dwordx4 v10, v[204:207], s[14:15] offset:0 nt
	s_waitcnt vmcnt(47)
	v_pk_mul_f32 v[208:209], v[42:43], v[208:209]
	v_pk_mul_f32 v[210:211], v[42:43], v[210:211]
	v_pk_mul_f32 v[208:209], v[80:81], v[208:209]
	v_pk_mul_f32 v[210:211], v[82:83], v[210:211]
	global_store_dwordx4 v10, v[208:211], s[14:15] offset:1024 nt
	s_waitcnt vmcnt(47)
	v_pk_mul_f32 v[212:213], v[42:43], v[212:213]
	v_pk_mul_f32 v[214:215], v[42:43], v[214:215]
	v_pk_mul_f32 v[212:213], v[84:85], v[212:213]
	v_pk_mul_f32 v[214:215], v[86:87], v[214:215]
	global_store_dwordx4 v10, v[212:215], s[14:15] offset:2048 nt
	s_waitcnt vmcnt(47)
	v_pk_mul_f32 v[216:217], v[42:43], v[216:217]
	v_pk_mul_f32 v[218:219], v[42:43], v[218:219]
	v_pk_mul_f32 v[216:217], v[88:89], v[216:217]
	v_pk_mul_f32 v[218:219], v[90:91], v[218:219]
	global_store_dwordx4 v10, v[216:219], s[14:15] offset:3072 nt
	s_waitcnt vmcnt(47)
	v_pk_mul_f32 v[220:221], v[42:43], v[220:221]
	v_pk_mul_f32 v[222:223], v[42:43], v[222:223]
	v_pk_mul_f32 v[220:221], v[92:93], v[220:221]
	v_pk_mul_f32 v[222:223], v[94:95], v[222:223]
	global_store_dwordx4 v11, v[220:223], s[14:15] offset:0 nt
	s_waitcnt vmcnt(47)
; __device__ __forceinline__ void p12_peer(Frame& F) {
;     ...
;           for (int c0 = 0; c0 < 16; c0 += 8) {
; #pragma unroll
;               for (int c = c0; c < c0 + 8; ++c) { const size_t col = (size_t)t * D_ + (size_t)(unsigned)(256 * c + lo2_); const f32x4 gn = *(const f32x4*)(lnf + (256 * c + lo2_));
;                   const f32x4 o = *(const f32x4*)(F.out + col);
;                   *(f32x4*)(F.out + col) = (f32x4){o.x * rs * gn.x, o.y * rs * gn.y, o.z * rs * gn.z, o.w * rs * gn.w}; }
;               asm volatile("" ::: "memory"); } }
	v_pk_mul_f32 v[224:225], v[42:43], v[224:225]
	v_pk_mul_f32 v[226:227], v[42:43], v[226:227]
	v_pk_mul_f32 v[224:225], v[96:97], v[224:225]
	v_pk_mul_f32 v[226:227], v[98:99], v[226:227]
	global_store_dwordx4 v11, v[224:227], s[14:15] offset:1024 nt
	s_waitcnt vmcnt(47)
	v_pk_mul_f32 v[228:229], v[42:43], v[228:229]
	v_pk_mul_f32 v[230:231], v[42:43], v[230:231]
	v_pk_mul_f32 v[228:229], v[100:101], v[228:229]
	v_pk_mul_f32 v[230:231], v[102:103], v[230:231]
	global_store_dwordx4 v11, v[228:231], s[14:15] offset:2048 nt
	s_waitcnt vmcnt(47)
	v_pk_mul_f32 v[232:233], v[42:43], v[232:233]
	v_pk_mul_f32 v[234:235], v[42:43], v[234:235]
	v_pk_mul_f32 v[232:233], v[104:105], v[232:233]
	v_pk_mul_f32 v[234:235], v[106:107], v[234:235]
	global_store_dwordx4 v11, v[232:235], s[14:15] offset:3072 nt
	s_waitcnt vmcnt(47)
	v_pk_mul_f32 v[236:237], v[42:43], v[236:237]
	v_pk_mul_f32 v[238:239], v[42:43], v[238:239]
	v_pk_mul_f32 v[236:237], v[108:109], v[236:237]
	v_pk_mul_f32 v[238:239], v[110:111], v[238:239]
	global_store_dwordx4 v12, v[236:239], s[14:15] offset:0 nt
	s_waitcnt vmcnt(47)
	v_pk_mul_f32 v[240:241], v[42:43], v[240:241]
	v_pk_mul_f32 v[242:243], v[42:43], v[242:243]
	v_pk_mul_f32 v[240:241], v[112:113], v[240:241]
	v_pk_mul_f32 v[242:243], v[114:115], v[242:243]
	global_store_dwordx4 v12, v[240:243], s[14:15] offset:1024 nt
	s_waitcnt vmcnt(47)
	v_pk_mul_f32 v[244:245], v[42:43], v[244:245]
	v_pk_mul_f32 v[246:247], v[42:43], v[246:247]
	v_pk_mul_f32 v[244:245], v[116:117], v[244:245]
	v_pk_mul_f32 v[246:247], v[118:119], v[246:247]
	global_store_dwordx4 v12, v[244:247], s[14:15] offset:2048 nt
	s_waitcnt vmcnt(47)
	v_pk_mul_f32 v[248:249], v[42:43], v[248:249]
	v_pk_mul_f32 v[250:251], v[42:43], v[250:251]
	v_pk_mul_f32 v[248:249], v[120:121], v[248:249]
	v_pk_mul_f32 v[250:251], v[122:123], v[250:251]
	global_store_dwordx4 v12, v[248:251], s[14:15] offset:3072 nt
	s_nop 1
	global_load_dwordx4 v[188:191], v6, s[18:19] offset:0
	global_load_dwordx4 v[192:195], v6, s[18:19] offset:1024
	global_load_dwordx4 v[196:199], v6, s[18:19] offset:2048
	global_load_dwordx4 v[200:203], v6, s[18:19] offset:3072
	global_load_dwordx4 v[204:207], v10, s[18:19] offset:0
	global_load_dwordx4 v[208:211], v10, s[18:19] offset:1024
	global_load_dwordx4 v[212:215], v10, s[18:19] offset:2048
	global_load_dwordx4 v[216:219], v10, s[18:19] offset:3072
	global_load_dwordx4 v[220:223], v11, s[18:19] offset:0
	global_load_dwordx4 v[224:227], v11, s[18:19] offset:1024
	global_load_dwordx4 v[228:231], v11, s[18:19] offset:2048
	global_load_dwordx4 v[232:235], v11, s[18:19] offset:3072
	global_load_dwordx4 v[236:239], v12, s[18:19] offset:0
	global_load_dwordx4 v[240:243], v12, s[18:19] offset:1024
	global_load_dwordx4 v[244:247], v12, s[18:19] offset:2048
	global_load_dwordx4 v[248:251], v12, s[18:19] offset:3072
	s_waitcnt vmcnt(47)
	v_pk_mul_f32 v[124:125], v[44:45], v[124:125]
	v_pk_mul_f32 v[126:127], v[44:45], v[126:127]
	v_pk_mul_f32 v[124:125], v[60:61], v[124:125]
	v_pk_mul_f32 v[126:127], v[62:63], v[126:127]
	global_store_dwordx4 v6, v[124:127], s[16:17] offset:0 nt
	s_waitcnt vmcnt(47)
	v_pk_mul_f32 v[128:129], v[44:45], v[128:129]
	v_pk_mul_f32 v[130:131], v[44:45], v[130:131]
	v_pk_mul_f32 v[128:129], v[64:65], v[128:129]
	v_pk_mul_f32 v[130:131], v[66:67], v[130:131]
	global_store_dwordx4 v6, v[128:131], s[16:17] offset:1024 nt
	s_waitcnt vmcnt(47)
	v_pk_mul_f32 v[132:133], v[44:45], v[132:133]
	v_pk_mul_f32 v[134:135], v[44:45], v[134:135]
	v_pk_mul_f32 v[132:133], v[68:69], v[132:133]
	v_pk_mul_f32 v[134:135], v[70:71], v[134:135]
	global_store_dwordx4 v6, v[132:135], s[16:17] offset:2048 nt
	s_waitcnt vmcnt(47)
	v_pk_mul_f32 v[136:137], v[44:45], v[136:137]
	v_pk_mul_f32 v[138:139], v[44:45], v[138:139]
	v_pk_mul_f32 v[136:137], v[72:73], v[136:137]
	v_pk_mul_f32 v[138:139], v[74:75], v[138:139]
	global_store_dwordx4 v6, v[136:139], s[16:17] offset:3072 nt
	s_waitcnt vmcnt(47)
	v_pk_mul_f32 v[140:141], v[44:45], v[140:141]
	v_pk_mul_f32 v[142:143], v[44:45], v[142:143]
	v_pk_mul_f32 v[140:141], v[76:77], v[140:141]
	v_pk_mul_f32 v[142:143], v[78:79], v[142:143]
	global_store_dwordx4 v10, v[140:143], s[16:17] offset:0 nt
	s_waitcnt vmcnt(47)
	v_pk_mul_f32 v[144:145], v[44:45], v[144:145]
	v_pk_mul_f32 v[146:147], v[44:45], v[146:147]
	v_pk_mul_f32 v[144:145], v[80:81], v[144:145]
	v_pk_mul_f32 v[146:147], v[82:83], v[146:147]
	global_store_dwordx4 v10, v[144:147], s[16:17] offset:1024 nt
	s_waitcnt vmcnt(47)
	v_pk_mul_f32 v[148:149], v[44:45], v[148:149]
	v_pk_mul_f32 v[150:151], v[44:45], v[150:151]
	v_pk_mul_f32 v[148:149], v[84:85], v[148:149]
	v_pk_mul_f32 v[150:151], v[86:87], v[150:151]
	global_store_dwordx4 v10, v[148:151], s[16:17] offset:2048 nt
	s_waitcnt vmcnt(47)
	v_pk_mul_f32 v[152:153], v[44:45], v[152:153]
	v_pk_mul_f32 v[154:155], v[44:45], v[154:155]
	v_pk_mul_f32 v[152:153], v[88:89], v[152:153]
	v_pk_mul_f32 v[154:155], v[90:91], v[154:155]
	global_store_dwordx4 v10, v[152:155], s[16:17] offset:3072 nt
	s_waitcnt vmcnt(47)
	v_pk_mul_f32 v[156:157], v[44:45], v[156:157]
	v_pk_mul_f32 v[158:159], v[44:45], v[158:159]
	v_pk_mul_f32 v[156:157], v[92:93], v[156:157]
	v_pk_mul_f32 v[158:159], v[94:95], v[158:159]
	global_store_dwordx4 v11, v[156:159], s[16:17] offset:0 nt
	s_waitcnt vmcnt(47)
	v_pk_mul_f32 v[160:161], v[44:45], v[160:161]
	v_pk_mul_f32 v[162:163], v[44:45], v[162:163]
	v_pk_mul_f32 v[160:161], v[96:97], v[160:161]
	v_pk_mul_f32 v[162:163], v[98:99], v[162:163]
	global_store_dwordx4 v11, v[160:163], s[16:17] offset:1024 nt
	s_waitcnt vmcnt(47)
; __device__ __forceinline__ void p12_peer(Frame& F) {
;     ...
;           for (int c0 = 0; c0 < 16; c0 += 8) {
; #pragma unroll
;               for (int c = c0; c < c0 + 8; ++c) { const size_t col = (size_t)t * D_ + (size_t)(unsigned)(256 * c + lo2_); const f32x4 gn = *(const f32x4*)(lnf + (256 * c + lo2_));
;                   const f32x4 o = *(const f32x4*)(F.out + col);
;                   *(f32x4*)(F.out + col) = (f32x4){o.x * rs * gn.x, o.y * rs * gn.y, o.z * rs * gn.z, o.w * rs * gn.w}; }
;               asm volatile("" ::: "memory"); } }
	v_pk_mul_f32 v[164:165], v[44:45], v[164:165]
	v_pk_mul_f32 v[166:167], v[44:45], v[166:167]
	v_pk_mul_f32 v[164:165], v[100:101], v[164:165]
	v_pk_mul_f32 v[166:167], v[102:103], v[166:167]
	global_store_dwordx4 v11, v[164:167], s[16:17] offset:2048 nt
	s_waitcnt vmcnt(47)
	v_pk_mul_f32 v[168:169], v[44:45], v[168:169]
	v_pk_mul_f32 v[170:171], v[44:45], v[170:171]
	v_pk_mul_f32 v[168:169], v[104:105], v[168:169]
	v_pk_mul_f32 v[170:171], v[106:107], v[170:171]
	global_store_dwordx4 v11, v[168:171], s[16:17] offset:3072 nt
	s_waitcnt vmcnt(47)
	v_pk_mul_f32 v[172:173], v[44:45], v[172:173]
	v_pk_mul_f32 v[174:175], v[44:45], v[174:175]
	v_pk_mul_f32 v[172:173], v[108:109], v[172:173]
	v_pk_mul_f32 v[174:175], v[110:111], v[174:175]
	global_store_dwordx4 v12, v[172:175], s[16:17] offset:0 nt
	s_waitcnt vmcnt(47)
	v_pk_mul_f32 v[176:177], v[44:45], v[176:177]
	v_pk_mul_f32 v[178:179], v[44:45], v[178:179]
	v_pk_mul_f32 v[176:177], v[112:113], v[176:177]
	v_pk_mul_f32 v[178:179], v[114:115], v[178:179]
	global_store_dwordx4 v12, v[176:179], s[16:17] offset:1024 nt
	s_waitcnt vmcnt(47)
	v_pk_mul_f32 v[180:181], v[44:45], v[180:181]
	v_pk_mul_f32 v[182:183], v[44:45], v[182:183]
	v_pk_mul_f32 v[180:181], v[116:117], v[180:181]
	v_pk_mul_f32 v[182:183], v[118:119], v[182:183]
	global_store_dwordx4 v12, v[180:183], s[16:17] offset:2048 nt
	s_waitcnt vmcnt(47)
	v_pk_mul_f32 v[184:185], v[44:45], v[184:185]
	v_pk_mul_f32 v[186:187], v[44:45], v[186:187]
	v_pk_mul_f32 v[184:185], v[120:121], v[184:185]
	v_pk_mul_f32 v[186:187], v[122:123], v[186:187]
	global_store_dwordx4 v12, v[184:187], s[16:17] offset:3072 nt
	s_waitcnt vmcnt(31)
	v_pk_mul_f32 v[188:189], v[46:47], v[188:189]
	v_pk_mul_f32 v[190:191], v[46:47], v[190:191]
	v_pk_mul_f32 v[188:189], v[60:61], v[188:189]
	v_pk_mul_f32 v[190:191], v[62:63], v[190:191]
	global_store_dwordx4 v6, v[188:191], s[18:19] offset:0 nt
	s_waitcnt vmcnt(31)
	v_pk_mul_f32 v[192:193], v[46:47], v[192:193]
	v_pk_mul_f32 v[194:195], v[46:47], v[194:195]
	v_pk_mul_f32 v[192:193], v[64:65], v[192:193]
	v_pk_mul_f32 v[194:195], v[66:67], v[194:195]
	global_store_dwordx4 v6, v[192:195], s[18:19] offset:1024 nt
	s_waitcnt vmcnt(31)
	v_pk_mul_f32 v[196:197], v[46:47], v[196:197]
	v_pk_mul_f32 v[198:199], v[46:47], v[198:199]
	v_pk_mul_f32 v[196:197], v[68:69], v[196:197]
	v_pk_mul_f32 v[198:199], v[70:71], v[198:199]
	global_store_dwordx4 v6, v[196:199], s[18:19] offset:2048 nt
	s_waitcnt vmcnt(31)
	v_pk_mul_f32 v[200:201], v[46:47], v[200:201]
	v_pk_mul_f32 v[202:203], v[46:47], v[202:203]
	v_pk_mul_f32 v[200:201], v[72:73], v[200:201]
	v_pk_mul_f32 v[202:203], v[74:75], v[202:203]
	global_store_dwordx4 v6, v[200:203], s[18:19] offset:3072 nt
	s_waitcnt vmcnt(31)
	v_pk_mul_f32 v[204:205], v[46:47], v[204:205]
	v_pk_mul_f32 v[206:207], v[46:47], v[206:207]
	v_pk_mul_f32 v[204:205], v[76:77], v[204:205]
	v_pk_mul_f32 v[206:207], v[78:79], v[206:207]
	global_store_dwordx4 v10, v[204:207], s[18:19] offset:0 nt
	s_waitcnt vmcnt(31)
	v_pk_mul_f32 v[208:209], v[46:47], v[208:209]
	v_pk_mul_f32 v[210:211], v[46:47], v[210:211]
	v_pk_mul_f32 v[208:209], v[80:81], v[208:209]
	v_pk_mul_f32 v[210:211], v[82:83], v[210:211]
	global_store_dwordx4 v10, v[208:211], s[18:19] offset:1024 nt
	s_waitcnt vmcnt(31)
	v_pk_mul_f32 v[212:213], v[46:47], v[212:213]
	v_pk_mul_f32 v[214:215], v[46:47], v[214:215]
	v_pk_mul_f32 v[212:213], v[84:85], v[212:213]
	v_pk_mul_f32 v[214:215], v[86:87], v[214:215]
	global_store_dwordx4 v10, v[212:215], s[18:19] offset:2048 nt
	s_waitcnt vmcnt(31)
	v_pk_mul_f32 v[216:217], v[46:47], v[216:217]
	v_pk_mul_f32 v[218:219], v[46:47], v[218:219]
	v_pk_mul_f32 v[216:217], v[88:89], v[216:217]
	v_pk_mul_f32 v[218:219], v[90:91], v[218:219]
	global_store_dwordx4 v10, v[216:219], s[18:19] offset:3072 nt
	s_waitcnt vmcnt(31)
	v_pk_mul_f32 v[220:221], v[46:47], v[220:221]
	v_pk_mul_f32 v[222:223], v[46:47], v[222:223]
	v_pk_mul_f32 v[220:221], v[92:93], v[220:221]
	v_pk_mul_f32 v[222:223], v[94:95], v[222:223]
	global_store_dwordx4 v11, v[220:223], s[18:19] offset:0 nt
	s_waitcnt vmcnt(31)
	v_pk_mul_f32 v[224:225], v[46:47], v[224:225]
	v_pk_mul_f32 v[226:227], v[46:47], v[226:227]
	v_pk_mul_f32 v[224:225], v[96:97], v[224:225]
	v_pk_mul_f32 v[226:227], v[98:99], v[226:227]
	global_store_dwordx4 v11, v[224:227], s[18:19] offset:1024 nt
	s_waitcnt vmcnt(31)
	v_pk_mul_f32 v[228:229], v[46:47], v[228:229]
	v_pk_mul_f32 v[230:231], v[46:47], v[230:231]
	v_pk_mul_f32 v[228:229], v[100:101], v[228:229]
	v_pk_mul_f32 v[230:231], v[102:103], v[230:231]
	global_store_dwordx4 v11, v[228:231], s[18:19] offset:2048 nt
	s_waitcnt vmcnt(31)
	v_pk_mul_f32 v[232:233], v[46:47], v[232:233]
	v_pk_mul_f32 v[234:235], v[46:47], v[234:235]
	v_pk_mul_f32 v[232:233], v[104:105], v[232:233]
	v_pk_mul_f32 v[234:235], v[106:107], v[234:235]
	global_store_dwordx4 v11, v[232:235], s[18:19] offset:3072 nt
	s_waitcnt vmcnt(31)
	v_pk_mul_f32 v[236:237], v[46:47], v[236:237]
	v_pk_mul_f32 v[238:239], v[46:47], v[238:239]
	v_pk_mul_f32 v[236:237], v[108:109], v[236:237]
	v_pk_mul_f32 v[238:239], v[110:111], v[238:239]
	global_store_dwordx4 v12, v[236:239], s[18:19] offset:0 nt
	s_waitcnt vmcnt(31)
	v_pk_mul_f32 v[240:241], v[46:47], v[240:241]
	v_pk_mul_f32 v[242:243], v[46:47], v[242:243]
	v_pk_mul_f32 v[240:241], v[112:113], v[240:241]
	v_pk_mul_f32 v[242:243], v[114:115], v[242:243]
	global_store_dwordx4 v12, v[240:243], s[18:19] offset:1024 nt
	s_waitcnt vmcnt(31)
	v_pk_mul_f32 v[244:245], v[46:47], v[244:245]
	v_pk_mul_f32 v[246:247], v[46:47], v[246:247]
	v_pk_mul_f32 v[244:245], v[116:117], v[244:245]
	v_pk_mul_f32 v[246:247], v[118:119], v[246:247]
	global_store_dwordx4 v12, v[244:247], s[18:19] offset:2048 nt
	s_waitcnt vmcnt(31)
	v_pk_mul_f32 v[248:249], v[46:47], v[248:249]
	v_pk_mul_f32 v[250:251], v[46:47], v[250:251]
	v_pk_mul_f32 v[248:249], v[120:121], v[248:249]
	v_pk_mul_f32 v[250:251], v[122:123], v[250:251]
	global_store_dwordx4 v12, v[248:251], s[18:19] offset:3072 nt
